# grid barrier arrive spread over 32 groups of 8 blocks (was 8 groups of 32); 32 adds per release word
# baseline (speedup 1.0000x reference)
.LBB0_8:
	s_or_b64 exec, exec, s[0:1]
	s_waitcnt lgkmcnt(0)
	s_barrier
	s_add_u32 s84, s54, 0x4000
	s_getreg_b32 s0, hwreg(HW_REG_XCC_ID, 0, 4)
	s_addc_u32 s85, s55, 0
	s_and_b32 s86, s0, 15
	s_and_b32 s99, s89, 63
	s_lshl_b32 s99, s99, 7
	s_add_u32 s99, s99, 0x1000
	s_lshl_b32 s99, s99, 16
	s_and_b32 s98, s89, 31
	s_lshl_b32 s98, s98, 7
	s_or_b32 s99, s99, s98
	s_add_u32 s100, s54, 0x8000
	s_addc_u32 s101, s55, 0
	s_mov_b32 s98, s33
	v_cmp_ne_u32_e64 s[0:1], 0, v0
	v_cmp_eq_u32_e64 s[78:79], 0, v0
	s_nop 0
	v_writelane_b32 v253, s0, 34
	s_nop 1
	v_writelane_b32 v253, s1, 35
	s_and_saveexec_b64 s[0:1], s[78:79]
	s_cbranch_execz .LBB0_11
	s_mov_b64 s[4:5], exec
	v_mbcnt_lo_u32_b32 v1, s4, 0
	v_mbcnt_hi_u32_b32 v1, s5, v1
	v_cmp_eq_u32_e32 vcc, 0, v1
	s_and_b64 s[2:3], exec, vcc
	s_mov_b64 exec, s[2:3]
	s_cbranch_execz .LBB0_11
	s_lshl_b32 s2, s86, 8
	s_bcnt1_i32_b64 s3, s[4:5]
	v_mov_b32_e32 v1, s2
	v_mov_b32_e32 v2, s3
	global_atomic_add v1, v2, s[84:85] offset:1024

.LBB0_230:
	v_writelane_b32 v253, s40, 46
	s_cmp_gt_i32 s81, 1
	s_cselect_b64 s[4:5], -1, 0
	v_writelane_b32 v253, s41, 47
	v_writelane_b32 v253, s42, 48
	v_writelane_b32 v253, s43, 49
	v_writelane_b32 v253, s44, 50
	v_writelane_b32 v253, s45, 51
	v_writelane_b32 v253, s46, 52
	v_writelane_b32 v253, s47, 53
	v_writelane_b32 v253, s48, 54
	v_writelane_b32 v253, s49, 55
	v_writelane_b32 v253, s50, 56
	v_writelane_b32 v253, s51, 57
	v_writelane_b32 v253, s52, 58
	v_writelane_b32 v253, s53, 59
	s_and_b64 s[0:1], s[0:1], s[4:5]
	v_writelane_b32 v253, s54, 60
	s_andn2_b64 vcc, exec, s[0:1]
	v_writelane_b32 v253, s55, 61
	s_cbranch_vccnz .LBB0_284
	s_waitcnt vmcnt(0)
	s_barrier
	s_and_saveexec_b64 s[0:1], s[78:79]
	s_cbranch_execz .LBB0_283
	v_mov_b32_e32 v1, 0x22160
	s_waitcnt vmcnt(0) lgkmcnt(0)
	ds_read_b32 v2, v1
	v_mov_b32_e32 v3, 1
	v_mov_b32_e32 v4, s99
	v_and_b32_e32 v5, 0xffff, v4
	v_lshrrev_b32_e32 v6, 16, v4
	global_atomic_add v7, v5, v3, s[100:101] sc0
	buffer_inv sc1
	v_lshrrev_b32_e32 v8, 7, v5
	v_sub_u32_e32 v8, s98, v8
	v_add_u32_e32 v8, 31, v8
	v_lshrrev_b32_e32 v8, 5, v8
	v_mov_b32_e32 v9, s98
	v_min_u32_e32 v9, 32, v9
	v_mov_b32_e32 v10, 0
	s_waitcnt lgkmcnt(0)
	v_add_u32_e32 v2, 1, v2
	ds_write_b32 v1, v2
	v_mul_lo_u32 v8, v8, v2
	v_mul_lo_u32 v9, v9, v2
	s_waitcnt vmcnt(0)
	v_add_u32_e32 v7, 1, v7
	v_cmp_eq_u32_e32 vcc, v7, v8
	s_cbranch_vccz .Lgb_poll_0
	s_mov_b64 exec, -1
	v_mbcnt_lo_u32_b32 v4, -1, 0
	v_mbcnt_hi_u32_b32 v4, -1, v4
	v_lshlrev_b32_e32 v4, 7, v4
	v_add_u32_e32 v4, 0x1000, v4
	v_mov_b32_e32 v3, 1
	global_atomic_add v4, v3, s[100:101]
	s_mov_b64 exec, 1

.LBB0_306:
	s_cmp_gt_i32 s81, 2
	s_cselect_b64 s[4:5], -1, 0
	s_and_b64 s[0:1], s[0:1], s[4:5]
	s_andn2_b64 vcc, exec, s[0:1]
	s_cbranch_vccnz .LBB0_360
	s_waitcnt vmcnt(0)
	s_waitcnt vmcnt(0)
	s_barrier
	s_and_saveexec_b64 s[0:1], s[78:79]
	s_cbranch_execz .LBB0_359
	v_mov_b32_e32 v1, 0x22160
	s_waitcnt vmcnt(0) lgkmcnt(0)
	ds_read_b32 v2, v1
	v_mov_b32_e32 v3, 1
	v_mov_b32_e32 v4, s99
	v_and_b32_e32 v5, 0xffff, v4
	v_lshrrev_b32_e32 v6, 16, v4
	global_atomic_add v7, v5, v3, s[100:101] sc0
	buffer_inv sc1
	v_lshrrev_b32_e32 v8, 7, v5
	v_sub_u32_e32 v8, s98, v8
	v_add_u32_e32 v8, 31, v8
	v_lshrrev_b32_e32 v8, 5, v8
	v_mov_b32_e32 v9, s98
	v_min_u32_e32 v9, 32, v9
	v_mov_b32_e32 v10, 0
	s_waitcnt lgkmcnt(0)
	v_add_u32_e32 v2, 1, v2
	ds_write_b32 v1, v2
	v_mul_lo_u32 v8, v8, v2
	v_mul_lo_u32 v9, v9, v2
	s_waitcnt vmcnt(0)
	v_add_u32_e32 v7, 1, v7
	v_cmp_eq_u32_e32 vcc, v7, v8
	s_cbranch_vccz .Lgb_poll_1
	s_mov_b64 exec, -1
	v_mbcnt_lo_u32_b32 v4, -1, 0
	v_mbcnt_hi_u32_b32 v4, -1, v4
	v_lshlrev_b32_e32 v4, 7, v4
	v_add_u32_e32 v4, 0x1000, v4
	v_mov_b32_e32 v3, 1
	global_atomic_add v4, v3, s[100:101]
	s_mov_b64 exec, 1

.LBB0_427:
	s_cmp_gt_i32 s81, 3
	s_cselect_b64 s[4:5], -1, 0
	s_and_b64 s[6:7], s[36:37], s[4:5]
	s_andn2_b64 vcc, exec, s[6:7]
	s_cbranch_vccnz .LBB0_481
	s_waitcnt vmcnt(0)
	s_waitcnt vmcnt(0)
	s_barrier
	s_and_saveexec_b64 s[6:7], s[78:79]
	s_cbranch_execz .LBB0_480
	v_mov_b32_e32 v1, 0x22160
	s_waitcnt vmcnt(0) lgkmcnt(0)
	ds_read_b32 v2, v1
	v_mov_b32_e32 v3, 1
	v_mov_b32_e32 v4, s99
	v_and_b32_e32 v5, 0xffff, v4
	v_lshrrev_b32_e32 v6, 16, v4
	global_atomic_add v7, v5, v3, s[100:101] sc0
	buffer_inv sc1
	v_lshrrev_b32_e32 v8, 7, v5
	v_sub_u32_e32 v8, s98, v8
	v_add_u32_e32 v8, 31, v8
	v_lshrrev_b32_e32 v8, 5, v8
	v_mov_b32_e32 v9, s98
	v_min_u32_e32 v9, 32, v9
	v_mov_b32_e32 v10, 0
	s_waitcnt lgkmcnt(0)
	v_add_u32_e32 v2, 1, v2
	ds_write_b32 v1, v2
	v_mul_lo_u32 v8, v8, v2
	v_mul_lo_u32 v9, v9, v2
	s_waitcnt vmcnt(0)
	v_add_u32_e32 v7, 1, v7
	v_cmp_eq_u32_e32 vcc, v7, v8
	s_cbranch_vccz .Lgb_chk_2
	s_mov_b64 exec, -1
	v_mbcnt_lo_u32_b32 v4, -1, 0
	v_mbcnt_hi_u32_b32 v4, -1, v4
	v_lshlrev_b32_e32 v4, 7, v4
	v_add_u32_e32 v4, 0x1000, v4
	v_mov_b32_e32 v3, 1
	global_atomic_add v4, v3, s[100:101]
	s_mov_b64 exec, 1

.LBB0_601:
	s_andn2_b64 vcc, exec, s[10:11]
	s_mov_b32 s46, s9
	s_cbranch_vccnz .LBB0_655
	s_waitcnt vmcnt(0)
	s_barrier
	s_mov_b64 s[10:11], exec
	v_readlane_b32 s44, v254, 12
	v_readlane_b32 s45, v254, 13
	s_and_b64 s[44:45], s[10:11], s[44:45]
	s_mov_b64 exec, s[44:45]
	s_cbranch_execz .LBB0_654
	v_mov_b32_e32 v7, v254
	v_cmp_gt_u32_e32 vcc, 0x88, v7
	s_cbranch_vccnz .Lgw_end_2
	v_mov_b32_e32 v8, 0x22160
	ds_read_b32 v9, v8
	v_mov_b32_e32 v10, s99
	v_lshrrev_b32_e32 v11, 16, v10
	v_mov_b32_e32 v12, s98
	v_min_u32_e32 v12, 32, v12
	v_mov_b32_e32 v13, 0
	s_waitcnt lgkmcnt(0)
	v_mul_lo_u32 v12, v12, v9

.Lgw_end_2:
	v_mov_b32_e32 v7, 0x22160
	s_waitcnt vmcnt(0) lgkmcnt(0)
	ds_read_b32 v8, v7
	v_mov_b32_e32 v9, 1
	v_mov_b32_e32 v10, s99
	v_and_b32_e32 v11, 0xffff, v10
	v_lshrrev_b32_e32 v12, 16, v10
	global_atomic_add v13, v11, v9, s[100:101] sc0
	buffer_inv sc1
	v_lshrrev_b32_e32 v14, 7, v11
	v_sub_u32_e32 v14, s98, v14
	v_add_u32_e32 v14, 31, v14
	v_lshrrev_b32_e32 v14, 5, v14
	v_mov_b32_e32 v15, s98
	v_min_u32_e32 v15, 32, v15
	v_mov_b32_e32 v16, 0
	s_waitcnt lgkmcnt(0)
	v_add_u32_e32 v8, 1, v8
	ds_write_b32 v7, v8
	v_mul_lo_u32 v14, v14, v8
	v_mul_lo_u32 v15, v15, v8
	s_waitcnt vmcnt(0)
	v_add_u32_e32 v13, 1, v13
	v_cmp_eq_u32_e32 vcc, v13, v14
	s_cbranch_vccz .Lgb_done_3
	s_mov_b64 exec, -1
	v_mbcnt_lo_u32_b32 v10, -1, 0
	v_mbcnt_hi_u32_b32 v10, -1, v10
	v_lshlrev_b32_e32 v10, 7, v10
	v_add_u32_e32 v10, 0x1000, v10
	v_mov_b32_e32 v9, 1
	global_atomic_add v10, v9, s[100:101]
	s_mov_b64 exec, 1

.LBB0_683:
	s_or_b64 exec, exec, s[56:57]
	s_waitcnt vmcnt(0)
	v_cndmask_b32_e64 v8, 0, 1, s[12:13]
	v_cmp_ne_u32_e64 s[56:57], 1, v8
	s_andn2_b64 vcc, exec, s[12:13]
	s_mov_b32 s45, 1
	s_cbranch_vccnz .LBB0_687
	v_readlane_b32 s58, v254, 12
	v_readlane_b32 s59, v254, 13
	s_and_saveexec_b64 s[12:13], s[58:59]
	s_cbranch_execz .Lgw_end_3
	v_mov_b32_e32 v8, 0x22160
	ds_read_b32 v9, v8
	v_mov_b32_e32 v10, s99
	v_lshrrev_b32_e32 v11, 16, v10
	v_mov_b32_e32 v12, s98
	v_min_u32_e32 v12, 32, v12
	v_mov_b32_e32 v13, 0
	s_waitcnt lgkmcnt(0)
	v_mul_lo_u32 v12, v12, v9

.LBB0_759:
	s_cmp_gt_i32 s81, 4
	s_cselect_b64 s[0:1], -1, 0
	s_and_b64 s[4:5], s[4:5], s[0:1]
	s_andn2_b64 vcc, exec, s[4:5]
	s_cbranch_vccnz .LBB0_813
	s_waitcnt vmcnt(0)
	s_waitcnt vmcnt(0)
	s_barrier
	s_and_saveexec_b64 s[4:5], s[78:79]
	s_cbranch_execz .LBB0_812
	v_mov_b32_e32 v1, 0x22160
	s_waitcnt vmcnt(0) lgkmcnt(0)
	ds_read_b32 v2, v1
	v_mov_b32_e32 v3, 1
	v_mov_b32_e32 v4, s99
	v_and_b32_e32 v5, 0xffff, v4
	v_lshrrev_b32_e32 v6, 16, v4
	global_atomic_add v7, v5, v3, s[100:101] sc0
	buffer_inv sc1
	v_lshrrev_b32_e32 v8, 7, v5
	v_sub_u32_e32 v8, s98, v8
	v_add_u32_e32 v8, 31, v8
	v_lshrrev_b32_e32 v8, 5, v8
	v_mov_b32_e32 v9, s98
	v_min_u32_e32 v9, 32, v9
	v_mov_b32_e32 v10, 0
	s_waitcnt lgkmcnt(0)
	v_add_u32_e32 v2, 1, v2
	ds_write_b32 v1, v2
	v_mul_lo_u32 v8, v8, v2
	v_mul_lo_u32 v9, v9, v2
	s_waitcnt vmcnt(0)
	v_add_u32_e32 v7, 1, v7
	v_cmp_eq_u32_e32 vcc, v7, v8
	s_cbranch_vccz .Lgb_chk_4
	s_mov_b64 exec, -1
	v_mbcnt_lo_u32_b32 v4, -1, 0
	v_mbcnt_hi_u32_b32 v4, -1, v4
	v_lshlrev_b32_e32 v4, 7, v4
	v_add_u32_e32 v4, 0x1000, v4
	v_mov_b32_e32 v3, 1
	global_atomic_add v4, v3, s[100:101]
	s_mov_b64 exec, 1

.LBB0_817:
	v_add_u32_e32 v12, s6, v222
	v_ashrrev_i32_e32 v13, 31, v12
	v_lshlrev_b64 v[12:13], 11, v[12:13]
	v_lshl_add_u64 v[56:57], v[4:5], 0, v[12:13]
	v_add_co_u32_e32 v58, vcc, 0x8000, v56
	global_load_dwordx4 v[12:15], v[56:57], off
	global_load_dwordx4 v[16:19], v[2:3], off
	v_addc_co_u32_e32 v59, vcc, 0, v57, vcc
	v_add_co_u32_e32 v60, vcc, 0x10000, v56
	global_load_dwordx4 v[20:23], v[58:59], off
	s_nop 0
	v_addc_co_u32_e32 v61, vcc, 0, v57, vcc
	v_add_co_u32_e32 v62, vcc, 0x18000, v56
	global_load_dwordx4 v[24:27], v[60:61], off
	s_nop 0
	v_addc_co_u32_e32 v63, vcc, 0, v57, vcc
	global_load_dwordx4 v[28:31], v[62:63], off
	global_load_dwordx4 v[32:35], v[56:57], off offset:64
	global_load_dwordx4 v[36:39], v[2:3], off offset:64
	global_load_dwordx4 v[40:43], v[58:59], off offset:64
	global_load_dwordx4 v[44:47], v[60:61], off offset:64
	global_load_dwordx4 v[48:51], v[62:63], off offset:64
	s_and_b64 vcc, exec, s[4:5]
	s_waitcnt vmcnt(8)
	v_mfma_f32_16x16x32_bf16 v[12:15], v[12:15], v[16:19], 0
	s_waitcnt vmcnt(7)
	v_mfma_f32_16x16x32_bf16 v[20:23], v[20:23], v[16:19], 0
	s_waitcnt vmcnt(6)
	v_mfma_f32_16x16x32_bf16 v[24:27], v[24:27], v[16:19], 0
	s_waitcnt vmcnt(5)
	v_mfma_f32_16x16x32_bf16 v[16:19], v[28:31], v[16:19], 0
	global_load_dwordx4 v[28:31], v[56:57], off offset:128
	global_load_dwordx4 v[52:55], v[2:3], off offset:128
	s_waitcnt vmcnt(5)
	v_mfma_f32_16x16x32_bf16 v[12:15], v[32:35], v[36:39], v[12:15]
	global_load_dwordx4 v[32:35], v[58:59], off offset:128
	s_waitcnt vmcnt(5)
	v_mfma_f32_16x16x32_bf16 v[20:23], v[40:43], v[36:39], v[20:23]
	global_load_dwordx4 v[40:43], v[60:61], off offset:128
	s_waitcnt vmcnt(5)
	v_mfma_f32_16x16x32_bf16 v[24:27], v[44:47], v[36:39], v[24:27]
	global_load_dwordx4 v[44:47], v[62:63], off offset:128
	s_waitcnt vmcnt(5)
	v_mfma_f32_16x16x32_bf16 v[16:19], v[48:51], v[36:39], v[16:19]
	global_load_dwordx4 v[36:39], v[56:57], off offset:192
	global_load_dwordx4 v[48:51], v[2:3], off offset:192
	s_waitcnt vmcnt(5)
	v_mfma_f32_16x16x32_bf16 v[12:15], v[28:31], v[52:55], v[12:15]
	global_load_dwordx4 v[28:31], v[58:59], off offset:192
	s_waitcnt vmcnt(5)
	v_mfma_f32_16x16x32_bf16 v[20:23], v[32:35], v[52:55], v[20:23]
	global_load_dwordx4 v[32:35], v[60:61], off offset:192
	s_waitcnt vmcnt(5)
	v_mfma_f32_16x16x32_bf16 v[24:27], v[40:43], v[52:55], v[24:27]
	global_load_dwordx4 v[40:43], v[62:63], off offset:192
	s_barrier
	s_waitcnt vmcnt(5)
	v_mfma_f32_16x16x32_bf16 v[16:19], v[44:47], v[52:55], v[16:19]
	s_waitcnt vmcnt(3)
	v_mfma_f32_16x16x32_bf16 v[12:15], v[36:39], v[48:51], v[12:15]
	s_waitcnt vmcnt(2)
	v_mfma_f32_16x16x32_bf16 v[20:23], v[28:31], v[48:51], v[20:23]
	s_waitcnt vmcnt(1)
	v_mfma_f32_16x16x32_bf16 v[24:27], v[32:35], v[48:51], v[24:27]
	s_waitcnt vmcnt(0)
	v_mfma_f32_16x16x32_bf16 v[16:19], v[40:43], v[48:51], v[16:19]
	s_nop 1
	ds_write_b128 v11, v[12:15]
	s_nop 0
	ds_write_b128 v11, v[20:23] offset:1024
	s_nop 0
	ds_write_b128 v11, v[24:27] offset:2048
	s_nop 0
	ds_write_b128 v11, v[16:19] offset:3072
	s_waitcnt lgkmcnt(0)
	s_barrier
	s_cbranch_vccnz .LBB0_816
	v_add_u32_e32 v80, s6, v10
	v_ashrrev_i32_e32 v81, 31, v80
	v_lshl_add_u64 v[82:83], v[80:81], 2, v[6:7]
	global_load_dwordx4 v[12:15], v[82:83], off
	global_load_dwordx4 v[88:91], v[82:83], off offset:64
	global_load_dwordx4 v[92:95], v[82:83], off offset:128
	global_load_dwordx4 v[96:99], v[82:83], off offset:192
	ds_read_b128 v[16:19], v1
	ds_read_b128 v[20:23], v1 offset:1024
	ds_read_b128 v[24:27], v1 offset:4096
	ds_read_b128 v[28:31], v1 offset:5120
	ds_read_b128 v[32:35], v1 offset:8192
	ds_read_b128 v[36:39], v1 offset:9216
	ds_read_b128 v[40:43], v1 offset:12288
	ds_read_b128 v[44:47], v1 offset:13312
	ds_read_b128 v[48:51], v1 offset:16384
	ds_read_b128 v[52:55], v1 offset:17408
	ds_read_b128 v[56:59], v1 offset:20480
	ds_read_b128 v[60:63], v1 offset:21504
	ds_read_b128 v[64:67], v1 offset:24576
	ds_read_b128 v[68:71], v1 offset:25600
	ds_read_b128 v[72:75], v1 offset:28672
	ds_read_b128 v[76:79], v1 offset:29696
	s_waitcnt lgkmcnt(13)
	v_pk_add_f32 v[18:19], v[18:19], v[26:27]
	v_pk_add_f32 v[16:17], v[16:17], v[24:25]
	s_waitcnt lgkmcnt(11)
	v_pk_add_f32 v[18:19], v[18:19], v[34:35]
	v_pk_add_f32 v[16:17], v[16:17], v[32:33]
	s_waitcnt lgkmcnt(9)
	v_pk_add_f32 v[18:19], v[18:19], v[42:43]
	v_pk_add_f32 v[16:17], v[16:17], v[40:41]
	s_waitcnt lgkmcnt(7)
	v_pk_add_f32 v[18:19], v[18:19], v[50:51]
	v_pk_add_f32 v[16:17], v[16:17], v[48:49]
	s_waitcnt lgkmcnt(5)
	v_pk_add_f32 v[18:19], v[18:19], v[58:59]
	v_pk_add_f32 v[16:17], v[16:17], v[56:57]
	s_waitcnt lgkmcnt(3)
	v_pk_add_f32 v[18:19], v[18:19], v[66:67]
	v_pk_add_f32 v[16:17], v[16:17], v[64:65]
	s_waitcnt lgkmcnt(1)
	v_pk_add_f32 v[18:19], v[18:19], v[74:75]
	v_pk_add_f32 v[16:17], v[16:17], v[72:73]
	v_lshl_add_u64 v[84:85], v[80:81], 1, v[8:9]
	v_pk_add_f32 v[20:21], v[20:21], v[28:29]
	s_waitcnt vmcnt(3)
	v_pk_add_f32 v[14:15], v[18:19], v[14:15]
	v_pk_add_f32 v[12:13], v[16:17], v[12:13]
	v_bfe_u32 v18, v14, 16, 1
	v_bfe_u32 v16, v12, 16, 1
	v_bfe_u32 v17, v13, 16, 1
	v_bfe_u32 v19, v15, 16, 1
	v_add3_u32 v12, v12, v16, s8
	v_add3_u32 v14, v14, v18, s8
	v_add3_u32 v13, v13, v17, s8
	v_add3_u32 v15, v15, v19, s8
	v_lshrrev_b32_e32 v12, 16, v12
	v_lshrrev_b32_e32 v14, 16, v14
	v_and_or_b32 v12, v13, s9, v12
	v_and_or_b32 v13, v15, s9, v14
	s_mov_b64 exec, 1
	v_mov_b32_e32 v24, 0x22160
	ds_read_b32 v25, v24
	v_mov_b32_e32 v26, s99
	v_lshrrev_b32_e32 v27, 16, v26
	v_mov_b32_e32 v32, s98
	v_min_u32_e32 v32, 32, v32
	v_mov_b32_e32 v33, 0
	s_waitcnt lgkmcnt(0)
	v_mul_lo_u32 v32, v32, v25

.LBB0_843:
	s_cmp_gt_i32 s81, 5
	s_cselect_b64 s[4:5], -1, 0
	s_and_b64 s[0:1], s[0:1], s[4:5]
	s_andn2_b64 vcc, exec, s[0:1]
	s_cbranch_vccnz .LBB0_897
	s_waitcnt vmcnt(0)
	s_waitcnt vmcnt(0)
	s_barrier
	s_and_saveexec_b64 s[0:1], s[78:79]
	s_cbranch_execz .LBB0_896
	v_mov_b32_e32 v1, 0x22160
	s_waitcnt vmcnt(0) lgkmcnt(0)
	ds_read_b32 v2, v1
	v_mov_b32_e32 v3, 1
	v_mov_b32_e32 v4, s99
	v_and_b32_e32 v5, 0xffff, v4
	v_lshrrev_b32_e32 v6, 16, v4
	global_atomic_add v7, v5, v3, s[100:101] sc0
	buffer_inv sc1
	v_lshrrev_b32_e32 v8, 7, v5
	v_sub_u32_e32 v8, s98, v8
	v_add_u32_e32 v8, 31, v8
	v_lshrrev_b32_e32 v8, 5, v8
	v_mov_b32_e32 v9, s98
	v_min_u32_e32 v9, 32, v9
	v_mov_b32_e32 v10, 0
	s_waitcnt lgkmcnt(0)
	v_add_u32_e32 v2, 1, v2
	ds_write_b32 v1, v2
	v_mul_lo_u32 v8, v8, v2
	v_mul_lo_u32 v9, v9, v2
	s_waitcnt vmcnt(0)
	v_add_u32_e32 v7, 1, v7
	v_cmp_eq_u32_e32 vcc, v7, v8
	s_cbranch_vccz .Lgb_done_5
	s_mov_b64 exec, -1
	v_mbcnt_lo_u32_b32 v4, -1, 0
	v_mbcnt_hi_u32_b32 v4, -1, v4
	v_lshlrev_b32_e32 v4, 7, v4
	v_add_u32_e32 v4, 0x1000, v4
	v_mov_b32_e32 v3, 1
	global_atomic_add v4, v3, s[100:101]
	s_mov_b64 exec, 1

.LBB0_906:
	s_or_b64 exec, exec, s[8:9]
	s_lshl_b32 s14, s95, 6
	v_or_b32_e32 v2, s14, v222
	v_ashrrev_i32_e32 v3, 31, v2
	v_lshlrev_b64 v[2:3], 11, v[2:3]
	v_and_b32_e32 v1, 48, v0
	v_lshl_add_u64 v[2:3], s[82:83], 0, v[2:3]
	v_lshl_or_b32 v18, s92, 8, v1
	v_mov_b32_e32 v19, 0
	v_lshl_add_u64 v[14:15], v[2:3], 0, v[18:19]
	s_and_saveexec_b64 s[8:9], s[78:79]
	s_cbranch_execz .Lgw_end_5
	v_mov_b32_e32 v1, 0x22160
	ds_read_b32 v2, v1
	v_mov_b32_e32 v3, s99
	v_lshrrev_b32_e32 v4, 16, v3
	v_mov_b32_e32 v5, s98
	v_min_u32_e32 v5, 32, v5
	v_mov_b32_e32 v6, 0
	s_waitcnt lgkmcnt(0)
	v_mul_lo_u32 v5, v5, v2

.LBB0_944:
	s_cmp_gt_i32 s81, 6
	s_cselect_b64 s[4:5], -1, 0
	s_and_b64 s[0:1], s[0:1], s[4:5]
	s_andn2_b64 vcc, exec, s[0:1]
	s_cbranch_vccnz .LBB0_998
	s_waitcnt vmcnt(0)
	s_waitcnt vmcnt(0)
	s_barrier
	s_and_saveexec_b64 s[0:1], s[78:79]
	s_cbranch_execz .LBB0_997
	v_mov_b32_e32 v1, 0x22160
	s_waitcnt vmcnt(0) lgkmcnt(0)
	ds_read_b32 v2, v1
	v_mov_b32_e32 v3, 1
	v_mov_b32_e32 v4, s99
	v_and_b32_e32 v5, 0xffff, v4
	v_lshrrev_b32_e32 v6, 16, v4
	global_atomic_add v7, v5, v3, s[100:101] sc0
	buffer_inv sc1
	v_lshrrev_b32_e32 v8, 7, v5
	v_sub_u32_e32 v8, s98, v8
	v_add_u32_e32 v8, 31, v8
	v_lshrrev_b32_e32 v8, 5, v8
	v_mov_b32_e32 v9, s98
	v_min_u32_e32 v9, 32, v9
	v_mov_b32_e32 v10, 0
	s_waitcnt lgkmcnt(0)
	v_add_u32_e32 v2, 1, v2
	ds_write_b32 v1, v2
	v_mul_lo_u32 v8, v8, v2
	v_mul_lo_u32 v9, v9, v2
	s_waitcnt vmcnt(0)
	v_add_u32_e32 v7, 1, v7
	v_cmp_eq_u32_e32 vcc, v7, v8
	s_cbranch_vccz .Lgb_poll_6
	s_mov_b64 exec, -1
	v_mbcnt_lo_u32_b32 v4, -1, 0
	v_mbcnt_hi_u32_b32 v4, -1, v4
	v_lshlrev_b32_e32 v4, 7, v4
	v_add_u32_e32 v4, 0x1000, v4
	v_mov_b32_e32 v3, 1
	global_atomic_add v4, v3, s[100:101]
	s_mov_b64 exec, 1

.Lcv_skip:
	s_cmp_gt_i32 s81, 7
	s_cselect_b64 s[4:5], -1, 0
	s_and_b64 s[0:1], s[76:77], s[4:5]
	v_readlane_b32 s86, v253, 40
	s_andn2_b64 vcc, exec, s[0:1]
	v_readlane_b32 s76, v253, 62
	v_readlane_b32 s77, v253, 63
	v_readlane_b32 s87, v253, 41
	s_cbranch_vccnz .LBB0_1205
	s_waitcnt vmcnt(0)
	s_waitcnt vmcnt(0) lgkmcnt(0)
	s_barrier
	s_and_saveexec_b64 s[0:1], s[78:79]
	s_cbranch_execz .LBB0_1204
	v_mov_b32_e32 v1, 0x22160
	s_waitcnt vmcnt(0) lgkmcnt(0)
	ds_read_b32 v2, v1
	v_mov_b32_e32 v3, 1
	v_mov_b32_e32 v4, s99
	v_and_b32_e32 v5, 0xffff, v4
	v_lshrrev_b32_e32 v6, 16, v4
	global_atomic_add v7, v5, v3, s[100:101] sc0
	buffer_inv sc1
	v_lshrrev_b32_e32 v8, 7, v5
	v_sub_u32_e32 v8, s98, v8
	v_add_u32_e32 v8, 31, v8
	v_lshrrev_b32_e32 v8, 5, v8
	v_mov_b32_e32 v9, s98
	v_min_u32_e32 v9, 32, v9
	v_mov_b32_e32 v10, 0
	s_waitcnt lgkmcnt(0)
	v_add_u32_e32 v2, 1, v2
	ds_write_b32 v1, v2
	v_mul_lo_u32 v8, v8, v2
	v_mul_lo_u32 v9, v9, v2
	s_waitcnt vmcnt(0)
	v_add_u32_e32 v7, 1, v7
	v_cmp_eq_u32_e32 vcc, v7, v8
	s_cbranch_vccz .Lgb_done_7
	s_mov_b64 exec, -1
	v_mbcnt_lo_u32_b32 v4, -1, 0
	v_mbcnt_hi_u32_b32 v4, -1, v4
	v_lshlrev_b32_e32 v4, 7, v4
	v_add_u32_e32 v4, 0x1000, v4
	v_mov_b32_e32 v3, 1
	global_atomic_add v4, v3, s[100:101]
	s_mov_b64 exec, 1

.LBB0_1210:
	global_load_dword v11, v[6:7], off
	global_load_dwordx4 v[12:15], v[8:9], off
	global_load_dwordx4 v[16:19], v[8:9], off offset:16
	global_load_dwordx4 v[20:23], v[8:9], off offset:32
	global_load_dwordx4 v[2:5], v[8:9], off offset:48
	v_add_co_u32_e32 v1, vcc, 0x200, v1
	s_xor_b64 s[16:17], vcc, -1
	s_and_b64 s[16:17], exec, s[16:17]
	v_lshl_add_u64 v[6:7], v[6:7], 0, s[6:7]
	v_lshl_add_u64 v[8:9], v[8:9], 0, s[8:9]
	s_or_b64 s[4:5], s[16:17], s[4:5]
	s_waitcnt vmcnt(0)
	v_mul_f32_e32 v24, v11, v12
	v_mul_f32_e32 v25, v11, v13
	v_mul_f32_e32 v26, v11, v14
	v_mul_f32_e32 v27, v11, v15
	v_mul_f32_e32 v28, v11, v16
	v_mul_f32_e32 v29, v11, v17
	v_mul_f32_e32 v30, v11, v18
	v_mul_f32_e32 v31, v11, v19
	v_mul_f32_e32 v32, v11, v20
	v_mul_f32_e32 v33, v11, v21
	v_mul_f32_e32 v34, v11, v22
	v_mul_f32_e32 v35, v11, v23
	v_mul_f32_e32 v36, v11, v2
	v_mul_f32_e32 v37, v11, v3
	v_mul_f32_e32 v38, v11, v4
	v_mul_f32_e32 v39, v11, v5
	v_bfe_u32 v40, v24, 16, 1
	v_bfe_u32 v41, v25, 16, 1
	v_bfe_u32 v42, v26, 16, 1
	v_bfe_u32 v43, v27, 16, 1
	v_bfe_u32 v44, v28, 16, 1
	v_bfe_u32 v45, v29, 16, 1
	v_bfe_u32 v46, v30, 16, 1
	v_bfe_u32 v47, v31, 16, 1
	v_bfe_u32 v48, v32, 16, 1
	v_bfe_u32 v49, v33, 16, 1
	v_bfe_u32 v50, v34, 16, 1
	v_bfe_u32 v51, v35, 16, 1
	v_bfe_u32 v52, v36, 16, 1
	v_bfe_u32 v53, v37, 16, 1
	v_bfe_u32 v54, v38, 16, 1
	v_bfe_u32 v55, v39, 16, 1
	v_add3_u32 v24, v24, v40, s14
	v_add3_u32 v25, v25, v41, s14
	v_add3_u32 v26, v26, v42, s14
	v_add3_u32 v27, v27, v43, s14
	v_add3_u32 v28, v28, v44, s14
	v_add3_u32 v29, v29, v45, s14
	v_add3_u32 v30, v30, v46, s14
	v_add3_u32 v31, v31, v47, s14
	v_add3_u32 v32, v32, v48, s14
	v_add3_u32 v33, v33, v49, s14
	v_add3_u32 v34, v34, v50, s14
	v_add3_u32 v35, v35, v51, s14
	v_add3_u32 v36, v36, v52, s14
	v_add3_u32 v37, v37, v53, s14
	v_add3_u32 v38, v38, v54, s14
	v_add3_u32 v39, v39, v55, s14
	ds_write_b16_d16_hi v10, v24
	v_and_b32_e32 v24, 0xffff0000, v24
	ds_write_b16_d16_hi v10, v25 offset:2048
	v_and_b32_e32 v25, 0xffff0000, v25
	ds_write_b16_d16_hi v10, v26 offset:4096
	v_and_b32_e32 v26, 0xffff0000, v26
	ds_write_b16_d16_hi v10, v27 offset:6144
	v_and_b32_e32 v27, 0xffff0000, v27
	ds_write_b16_d16_hi v10, v28 offset:8192
	v_and_b32_e32 v28, 0xffff0000, v28
	ds_write_b16_d16_hi v10, v29 offset:10240
	v_and_b32_e32 v29, 0xffff0000, v29
	ds_write_b16_d16_hi v10, v30 offset:12288
	v_and_b32_e32 v30, 0xffff0000, v30
	ds_write_b16_d16_hi v10, v31 offset:14336
	v_and_b32_e32 v31, 0xffff0000, v31
	ds_write_b16_d16_hi v10, v32 offset:16384
	v_and_b32_e32 v32, 0xffff0000, v32
	ds_write_b16_d16_hi v10, v33 offset:18432
	v_and_b32_e32 v33, 0xffff0000, v33
	ds_write_b16_d16_hi v10, v34 offset:20480
	v_and_b32_e32 v34, 0xffff0000, v34
	ds_write_b16_d16_hi v10, v35 offset:22528
	v_and_b32_e32 v35, 0xffff0000, v35
	ds_write_b16_d16_hi v10, v36 offset:24576
	v_and_b32_e32 v36, 0xffff0000, v36
	ds_write_b16_d16_hi v10, v37 offset:26624
	v_and_b32_e32 v37, 0xffff0000, v37
	ds_write_b16_d16_hi v10, v38 offset:28672
	v_and_b32_e32 v38, 0xffff0000, v38
	ds_write_b16_d16_hi v10, v39 offset:30720
	v_and_b32_e32 v39, 0xffff0000, v39
	v_fma_f32 v12, v11, v12, -v24
	v_fma_f32 v13, v11, v13, -v25
	v_fma_f32 v14, v11, v14, -v26
	v_fma_f32 v15, v11, v15, -v27
	v_fma_f32 v16, v11, v16, -v28
	v_fma_f32 v17, v11, v17, -v29
	v_fma_f32 v18, v11, v18, -v30
	v_fma_f32 v19, v11, v19, -v31
	v_fma_f32 v20, v11, v20, -v32
	v_fma_f32 v21, v11, v21, -v33
	v_fma_f32 v22, v11, v22, -v34
	v_fma_f32 v23, v11, v23, -v35
	v_fma_f32 v2, v11, v2, -v36
	v_fma_f32 v3, v11, v3, -v37
	v_fma_f32 v4, v11, v4, -v38
	v_fma_f32 v5, v11, v5, -v39
	v_bfe_u32 v11, v12, 16, 1
	v_bfe_u32 v24, v13, 16, 1
	v_bfe_u32 v25, v14, 16, 1
	v_bfe_u32 v26, v15, 16, 1
	v_bfe_u32 v27, v16, 16, 1
	v_bfe_u32 v28, v17, 16, 1
	v_bfe_u32 v29, v18, 16, 1
	v_bfe_u32 v30, v19, 16, 1
	v_bfe_u32 v31, v20, 16, 1
	v_bfe_u32 v32, v21, 16, 1
	v_bfe_u32 v33, v22, 16, 1
	v_bfe_u32 v34, v23, 16, 1
	v_bfe_u32 v35, v2, 16, 1
	v_bfe_u32 v36, v3, 16, 1
	v_bfe_u32 v37, v4, 16, 1
	v_bfe_u32 v38, v5, 16, 1
	v_add3_u32 v11, v12, v11, s14
	v_add3_u32 v12, v13, v24, s14
	v_add3_u32 v13, v14, v25, s14
	v_add3_u32 v14, v15, v26, s14
	v_add3_u32 v15, v16, v27, s14
	v_add3_u32 v16, v17, v28, s14
	v_add3_u32 v17, v18, v29, s14
	v_add3_u32 v18, v19, v30, s14
	v_add3_u32 v19, v20, v31, s14
	v_add3_u32 v20, v21, v32, s14
	v_add3_u32 v21, v22, v33, s14
	v_add3_u32 v22, v23, v34, s14
	v_add3_u32 v2, v2, v35, s14
	v_add3_u32 v3, v3, v36, s14
	v_add3_u32 v4, v4, v37, s14
	v_add3_u32 v5, v5, v38, s14
	ds_write_b16_d16_hi v10, v11 offset:32768
	ds_write_b16_d16_hi v10, v12 offset:34816
	ds_write_b16_d16_hi v10, v13 offset:36864
	ds_write_b16_d16_hi v10, v14 offset:38912
	ds_write_b16_d16_hi v10, v15 offset:40960
	ds_write_b16_d16_hi v10, v16 offset:43008
	ds_write_b16_d16_hi v10, v17 offset:45056
	ds_write_b16_d16_hi v10, v18 offset:47104
	ds_write_b16_d16_hi v10, v19 offset:49152
	ds_write_b16_d16_hi v10, v20 offset:51200
	ds_write_b16_d16_hi v10, v21 offset:53248
	ds_write_b16_d16_hi v10, v22 offset:55296
	ds_write_b16_d16_hi v10, v2 offset:57344
	ds_write_b16_d16_hi v10, v3 offset:59392
	ds_write_b16_d16_hi v10, v4 offset:61440
	ds_write_b16_d16_hi v10, v5 offset:63488
	v_add_u32_e32 v10, 0x400, v10
	s_andn2_b64 exec, exec, s[4:5]
	s_cbranch_execnz .LBB0_1210
	s_or_b64 exec, exec, s[4:5]
	s_and_saveexec_b64 s[4:5], s[78:79]
	s_cbranch_execz .Lgw_end_7
	v_mov_b32_e32 v1, 0x22160
	ds_read_b32 v2, v1
	v_mov_b32_e32 v3, s99
	v_lshrrev_b32_e32 v4, 16, v3
	v_mov_b32_e32 v5, s98
	v_min_u32_e32 v5, 32, v5
	v_mov_b32_e32 v6, 0
	s_waitcnt lgkmcnt(0)
	v_mul_lo_u32 v5, v5, v2

.LBB0_1220:
	s_cmp_gt_i32 s81, 8
	s_cselect_b64 s[14:15], -1, 0
	s_and_b64 s[4:5], s[12:13], s[14:15]
	s_andn2_b64 vcc, exec, s[4:5]
	s_cbranch_vccnz .LBB0_1274
	s_waitcnt vmcnt(0)
	s_waitcnt vmcnt(0) lgkmcnt(0)
	s_barrier
	s_and_saveexec_b64 s[4:5], s[78:79]
	s_cbranch_execz .LBB0_1273
	v_mov_b32_e32 v1, 0x22160
	s_waitcnt vmcnt(0) lgkmcnt(0)
	ds_read_b32 v2, v1
	v_mov_b32_e32 v3, 1
	v_mov_b32_e32 v4, s99
	v_and_b32_e32 v5, 0xffff, v4
	v_lshrrev_b32_e32 v6, 16, v4
	global_atomic_add v7, v5, v3, s[100:101] sc0
	buffer_inv sc1
	v_lshrrev_b32_e32 v8, 7, v5
	v_sub_u32_e32 v8, s98, v8
	v_add_u32_e32 v8, 31, v8
	v_lshrrev_b32_e32 v8, 5, v8
	v_mov_b32_e32 v9, s98
	v_min_u32_e32 v9, 32, v9
	v_mov_b32_e32 v10, 0
	s_waitcnt lgkmcnt(0)
	v_add_u32_e32 v2, 1, v2
	ds_write_b32 v1, v2
	v_mul_lo_u32 v8, v8, v2
	v_mul_lo_u32 v9, v9, v2
	s_waitcnt vmcnt(0)
	v_add_u32_e32 v7, 1, v7
	v_cmp_eq_u32_e32 vcc, v7, v8
	s_cbranch_vccz .Lgb_poll_8
	s_mov_b64 exec, -1
	v_mbcnt_lo_u32_b32 v4, -1, 0
	v_mbcnt_hi_u32_b32 v4, -1, v4
	v_lshlrev_b32_e32 v4, 7, v4
	v_add_u32_e32 v4, 0x1000, v4
	v_mov_b32_e32 v3, 1
	global_atomic_add v4, v3, s[100:101]
	s_mov_b64 exec, 1

.LBB0_1371:
	s_or_b64 exec, exec, s[4:5]
	s_waitcnt lgkmcnt(0)
	s_barrier
	s_and_saveexec_b64 s[4:5], s[6:7]
	s_cbranch_execz .LBB0_1373
	v_lshl_add_u32 v1, v0, 2, 0
	ds_read_b32 v1, v1 offset:128
	v_lshl_or_b32 v2, s18, 5, v0
	v_readlane_b32 s36, v253, 46
	v_ashrrev_i32_e32 v3, 31, v2
	v_readlane_b32 s50, v253, 60
	v_readlane_b32 s51, v253, 61
	s_waitcnt lgkmcnt(0)
	v_min_i32_e32 v1, v1, v252
	v_and_b32_e32 v1, -2, v1
	v_lshl_add_u64 v[2:3], v[2:3], 2, s[50:51]
	v_add_co_u32_e32 v2, vcc, 0x1582000, v2
	v_readlane_b32 s37, v253, 47
	s_nop 0
	v_addc_co_u32_e32 v3, vcc, 0, v3, vcc
	v_readlane_b32 s38, v253, 48
	v_readlane_b32 s39, v253, 49
	v_readlane_b32 s40, v253, 50
	v_readlane_b32 s41, v253, 51
	v_readlane_b32 s42, v253, 52
	v_readlane_b32 s43, v253, 53
	v_readlane_b32 s44, v253, 54
	v_readlane_b32 s45, v253, 55
	v_readlane_b32 s46, v253, 56
	v_readlane_b32 s47, v253, 57
	v_readlane_b32 s48, v253, 58
	v_readlane_b32 s49, v253, 59
	global_store_dword v[2:3], v1, off sc1
	s_waitcnt vmcnt(0)
	s_mov_b64 exec, 1
	v_mov_b32_e32 v2, 0
	v_mov_b32_e32 v3, 1
	global_atomic_add v2, v3, s[100:101] offset:4032

.LBB0_1606:
	s_cmp_gt_i32 s81, 10
	s_cselect_b64 s[0:1], -1, 0
	s_and_b64 s[4:5], s[12:13], s[0:1]
	s_andn2_b64 vcc, exec, s[4:5]
	s_waitcnt vmcnt(0)
	v_and_b32_e32 v82, 63, v0
	s_cbranch_vccnz .LBB0_1660
	s_waitcnt vmcnt(0)
	s_waitcnt lgkmcnt(0)
	s_barrier
	s_and_saveexec_b64 s[4:5], s[78:79]
	s_cbranch_execz .LBB0_1659
	v_mov_b32_e32 v1, 0x22160
	s_waitcnt vmcnt(0) lgkmcnt(0)
	ds_read_b32 v2, v1
	v_mov_b32_e32 v3, 1
	v_mov_b32_e32 v4, s99
	v_and_b32_e32 v5, 0xffff, v4
	v_lshrrev_b32_e32 v6, 16, v4
	global_atomic_add v7, v5, v3, s[100:101] sc0
	buffer_inv sc1
	v_mov_b32_e32 v12, 0
	global_load_dword v11, v12, s[100:101] offset:4032 sc1
	v_lshrrev_b32_e32 v8, 7, v5
	v_sub_u32_e32 v8, s98, v8
	v_add_u32_e32 v8, 31, v8
	v_lshrrev_b32_e32 v8, 5, v8
	v_mov_b32_e32 v9, s98
	v_min_u32_e32 v9, 32, v9
	v_mov_b32_e32 v10, 0
	s_waitcnt lgkmcnt(0)
	v_add_u32_e32 v2, 1, v2
	ds_write_b32 v1, v2
	v_mul_lo_u32 v8, v8, v2
	v_mul_lo_u32 v9, v9, v2
	s_waitcnt vmcnt(0)
	v_add_u32_e32 v7, 1, v7
	v_cmp_eq_u32_e32 vcc, v7, v8
	s_cbranch_vccz .Lgb_chk_9
	s_mov_b64 exec, -1
	v_mbcnt_lo_u32_b32 v4, -1, 0
	v_mbcnt_hi_u32_b32 v4, -1, v4
	v_lshlrev_b32_e32 v4, 7, v4
	v_add_u32_e32 v4, 0x1000, v4
	v_mov_b32_e32 v3, 1
	global_atomic_add v4, v3, s[100:101]
	s_mov_b64 exec, 1
.Lgb_chk_9:
	v_mov_b32_e32 v6, 0xfc0
	v_mov_b32_e32 v9, 32
	v_cmp_ge_u32_e32 vcc, v11, v9
	s_cbranch_vccnz .Lgb_done_9

.LBB0_1687:
	s_or_b64 exec, exec, s[6:7]
	v_add_u32_e32 v1, s30, v2
	ds_write_b32 v1, v3 offset:4
	v_add_u32_e32 v1, s30, v250
	s_waitcnt lgkmcnt(0)
	s_barrier
	ds_read_b128 v[8:11], v1
	v_cmp_eq_u32_e32 vcc, 0, v192
	s_waitcnt lgkmcnt(0)
	s_barrier
	v_and_b32_e32 v17, 0x80, v0
	v_and_b32_e32 v205, 31, v0
	s_waitcnt lgkmcnt(0)
	v_max_i32_e32 v2, v8, v9
	v_min_i32_e32 v6, v10, v11
	v_min_i32_e32 v3, v8, v9
	v_max_i32_e32 v5, v10, v11
	v_max_i32_e32 v8, v2, v6
	v_min_i32_e32 v2, v2, v6
	v_cndmask_b32_e32 v6, v2, v8, vcc
	v_cndmask_b32_e32 v2, v8, v2, vcc
	v_max_i32_e32 v8, v3, v5
	v_min_i32_e32 v3, v3, v5
	v_cndmask_b32_e32 v5, v3, v8, vcc
	v_cndmask_b32_e32 v3, v8, v3, vcc
	v_max_i32_e32 v8, v6, v5
	v_min_i32_e32 v5, v6, v5
	v_cndmask_b32_e32 v6, v5, v8, vcc
	v_cndmask_b32_e32 v5, v8, v5, vcc
	v_max_i32_e32 v9, v2, v3
	v_min_i32_e32 v3, v2, v3
	v_xor_b32_e32 v2, 1, v7
	v_add_u32_e32 v8, 64, v4
	v_cmp_lt_i32_e64 s[6:7], v2, v8
	v_cndmask_b32_e32 v10, v3, v9, vcc
	v_cndmask_b32_e32 v3, v9, v3, vcc
	v_cndmask_b32_e64 v2, v7, v2, s[6:7]
	v_lshlrev_b32_e32 v2, 2, v2
	ds_bpermute_b32 v4, v2, v6
	ds_bpermute_b32 v12, v2, v5
	v_and_b32_e32 v9, 2, v0
	v_cmp_ne_u32_e64 s[6:7], 0, v9
	s_xor_b64 s[6:7], vcc, s[6:7]
	s_waitcnt lgkmcnt(1)
	v_max_i32_e32 v11, v6, v4
	v_min_i32_e32 v4, v6, v4
	v_cndmask_b32_e64 v4, v4, v11, s[6:7]
	ds_bpermute_b32 v6, v2, v10
	s_waitcnt lgkmcnt(1)
	v_max_i32_e32 v11, v5, v12
	v_min_i32_e32 v5, v5, v12
	ds_bpermute_b32 v12, v2, v3
	v_cndmask_b32_e64 v5, v5, v11, s[6:7]
	s_waitcnt lgkmcnt(1)
	v_max_i32_e32 v11, v10, v6
	v_min_i32_e32 v6, v10, v6
	v_cndmask_b32_e64 v6, v6, v11, s[6:7]
	s_waitcnt lgkmcnt(0)
	v_max_i32_e32 v10, v3, v12
	v_min_i32_e32 v3, v3, v12
	v_cndmask_b32_e64 v3, v3, v10, s[6:7]
	v_max_i32_e32 v10, v4, v6
	v_min_i32_e32 v4, v4, v6
	v_cmp_eq_u32_e64 s[6:7], 0, v9
	v_max_i32_e32 v9, v5, v3
	v_min_i32_e32 v3, v5, v3
	v_cndmask_b32_e64 v6, v4, v10, s[6:7]
	v_cndmask_b32_e64 v5, v3, v9, s[6:7]
	v_cndmask_b32_e64 v4, v10, v4, s[6:7]
	v_cndmask_b32_e64 v3, v9, v3, s[6:7]
	v_max_i32_e32 v9, v6, v5
	v_min_i32_e32 v5, v6, v5
	v_cndmask_b32_e64 v6, v5, v9, s[6:7]
	v_cndmask_b32_e64 v5, v9, v5, s[6:7]
	v_max_i32_e32 v9, v4, v3
	v_min_i32_e32 v4, v4, v3
	v_xor_b32_e32 v3, 2, v7
	v_cmp_lt_i32_e64 s[8:9], v3, v8
	v_cndmask_b32_e64 v11, v4, v9, s[6:7]
	v_cndmask_b32_e64 v4, v9, v4, s[6:7]
	v_cndmask_b32_e64 v3, v7, v3, s[8:9]
	v_lshlrev_b32_e32 v3, 2, v3
	ds_bpermute_b32 v10, v3, v6
	ds_bpermute_b32 v13, v3, v5
	v_and_b32_e32 v9, 4, v0
	v_cmp_ne_u32_e64 s[8:9], 0, v9
	s_xor_b64 s[10:11], s[6:7], s[8:9]
	s_waitcnt lgkmcnt(1)
	v_max_i32_e32 v12, v6, v10
	v_min_i32_e32 v6, v6, v10
	v_cndmask_b32_e64 v6, v6, v12, s[10:11]
	ds_bpermute_b32 v10, v3, v11
	s_waitcnt lgkmcnt(1)
	v_max_i32_e32 v12, v5, v13
	v_min_i32_e32 v5, v5, v13
	v_cndmask_b32_e64 v5, v5, v12, s[10:11]
	ds_bpermute_b32 v12, v3, v4
	s_waitcnt lgkmcnt(1)
	v_max_i32_e32 v13, v11, v10
	v_min_i32_e32 v10, v11, v10
	ds_bpermute_b32 v11, v2, v6
	v_cndmask_b32_e64 v10, v10, v13, s[10:11]
	s_waitcnt lgkmcnt(1)
	v_max_i32_e32 v13, v4, v12
	v_min_i32_e32 v4, v4, v12
	v_cndmask_b32_e64 v4, v4, v13, s[10:11]
	ds_bpermute_b32 v13, v2, v5
	s_waitcnt lgkmcnt(1)
	v_max_i32_e32 v12, v6, v11
	v_min_i32_e32 v6, v6, v11
	s_xor_b64 s[8:9], vcc, s[8:9]
	v_cndmask_b32_e64 v6, v6, v12, s[8:9]
	ds_bpermute_b32 v11, v2, v10
	s_waitcnt lgkmcnt(1)
	v_max_i32_e32 v12, v5, v13
	v_min_i32_e32 v5, v5, v13
	ds_bpermute_b32 v13, v2, v4
	v_cndmask_b32_e64 v5, v5, v12, s[8:9]
	s_waitcnt lgkmcnt(1)
	v_max_i32_e32 v12, v10, v11
	v_min_i32_e32 v10, v10, v11
	v_cndmask_b32_e64 v10, v10, v12, s[8:9]
	s_waitcnt lgkmcnt(0)
	v_max_i32_e32 v11, v4, v13
	v_min_i32_e32 v4, v4, v13
	v_cndmask_b32_e64 v4, v4, v11, s[8:9]
	v_max_i32_e32 v11, v6, v10
	v_min_i32_e32 v6, v6, v10
	v_cmp_eq_u32_e64 s[8:9], 0, v9
	v_max_i32_e32 v10, v5, v4
	v_min_i32_e32 v4, v5, v4
	v_cndmask_b32_e64 v9, v6, v11, s[8:9]
	v_cndmask_b32_e64 v5, v4, v10, s[8:9]
	v_cndmask_b32_e64 v6, v11, v6, s[8:9]
	v_cndmask_b32_e64 v4, v10, v4, s[8:9]
	v_max_i32_e32 v10, v9, v5
	v_min_i32_e32 v5, v9, v5
	v_cndmask_b32_e64 v9, v5, v10, s[8:9]
	v_cndmask_b32_e64 v5, v10, v5, s[8:9]
	v_max_i32_e32 v10, v6, v4
	v_min_i32_e32 v6, v6, v4
	v_xor_b32_e32 v4, 4, v7
	v_cmp_lt_i32_e64 s[10:11], v4, v8
	v_cndmask_b32_e64 v12, v6, v10, s[8:9]
	v_cndmask_b32_e64 v6, v10, v6, s[8:9]
	v_cndmask_b32_e64 v4, v7, v4, s[10:11]
	v_lshlrev_b32_e32 v4, 2, v4
	ds_bpermute_b32 v11, v4, v9
	ds_bpermute_b32 v14, v4, v5
	v_and_b32_e32 v10, 8, v0
	v_cmp_ne_u32_e64 s[10:11], 0, v10
	s_xor_b64 s[12:13], s[8:9], s[10:11]
	s_waitcnt lgkmcnt(1)
	v_max_i32_e32 v13, v9, v11
	v_min_i32_e32 v9, v9, v11
	v_cndmask_b32_e64 v9, v9, v13, s[12:13]
	ds_bpermute_b32 v11, v4, v12
	s_waitcnt lgkmcnt(1)
	v_max_i32_e32 v13, v5, v14
	v_min_i32_e32 v5, v5, v14
	v_cndmask_b32_e64 v5, v5, v13, s[12:13]
	ds_bpermute_b32 v13, v4, v6
	s_waitcnt lgkmcnt(1)
	v_max_i32_e32 v14, v12, v11
	v_min_i32_e32 v11, v12, v11
	ds_bpermute_b32 v12, v3, v9
	v_cndmask_b32_e64 v11, v11, v14, s[12:13]
	s_waitcnt lgkmcnt(1)
	v_max_i32_e32 v14, v6, v13
	v_min_i32_e32 v6, v6, v13
	v_cndmask_b32_e64 v6, v6, v14, s[12:13]
	ds_bpermute_b32 v14, v3, v5
	s_waitcnt lgkmcnt(1)
	v_max_i32_e32 v13, v9, v12
	v_min_i32_e32 v9, v9, v12
	s_xor_b64 s[12:13], s[6:7], s[10:11]
	v_cndmask_b32_e64 v9, v9, v13, s[12:13]
	ds_bpermute_b32 v12, v3, v11
	s_waitcnt lgkmcnt(1)
	v_max_i32_e32 v13, v5, v14
	v_min_i32_e32 v5, v5, v14
	v_cndmask_b32_e64 v5, v5, v13, s[12:13]
	ds_bpermute_b32 v13, v3, v6
	s_waitcnt lgkmcnt(1)
	v_max_i32_e32 v14, v11, v12
	v_min_i32_e32 v11, v11, v12
	ds_bpermute_b32 v12, v2, v9
	v_cndmask_b32_e64 v11, v11, v14, s[12:13]
	s_waitcnt lgkmcnt(1)
	v_max_i32_e32 v14, v6, v13
	v_min_i32_e32 v6, v6, v13
	v_cndmask_b32_e64 v6, v6, v14, s[12:13]
	ds_bpermute_b32 v14, v2, v5
	s_waitcnt lgkmcnt(1)
	v_max_i32_e32 v13, v9, v12
	v_min_i32_e32 v9, v9, v12
	s_xor_b64 s[10:11], vcc, s[10:11]
	v_cndmask_b32_e64 v9, v9, v13, s[10:11]
	ds_bpermute_b32 v12, v2, v11
	s_waitcnt lgkmcnt(1)
	v_max_i32_e32 v13, v5, v14
	v_min_i32_e32 v5, v5, v14
	ds_bpermute_b32 v14, v2, v6
	v_cndmask_b32_e64 v5, v5, v13, s[10:11]
	s_waitcnt lgkmcnt(1)
	v_max_i32_e32 v13, v11, v12
	v_min_i32_e32 v11, v11, v12
	v_cndmask_b32_e64 v11, v11, v13, s[10:11]
	s_waitcnt lgkmcnt(0)
	v_max_i32_e32 v12, v6, v14
	v_min_i32_e32 v6, v6, v14
	v_cndmask_b32_e64 v6, v6, v12, s[10:11]
	v_max_i32_e32 v12, v9, v11
	v_min_i32_e32 v9, v9, v11
	v_cmp_eq_u32_e64 s[10:11], 0, v10
	v_max_i32_e32 v11, v5, v6
	v_min_i32_e32 v5, v5, v6
	v_cndmask_b32_e64 v10, v9, v12, s[10:11]
	v_cndmask_b32_e64 v6, v5, v11, s[10:11]
	v_cndmask_b32_e64 v9, v12, v9, s[10:11]
	v_cndmask_b32_e64 v5, v11, v5, s[10:11]
	v_max_i32_e32 v11, v10, v6
	v_min_i32_e32 v6, v10, v6
	v_cndmask_b32_e64 v10, v6, v11, s[10:11]
	v_cndmask_b32_e64 v6, v11, v6, s[10:11]
	v_max_i32_e32 v11, v9, v5
	v_min_i32_e32 v9, v9, v5
	v_xor_b32_e32 v5, 8, v7
	v_cmp_lt_i32_e64 s[12:13], v5, v8
	v_cndmask_b32_e64 v13, v9, v11, s[10:11]
	v_cndmask_b32_e64 v9, v11, v9, s[10:11]
	v_cndmask_b32_e64 v5, v7, v5, s[12:13]
	v_lshlrev_b32_e32 v5, 2, v5
	ds_bpermute_b32 v12, v5, v10
	ds_bpermute_b32 v15, v5, v6
	v_and_b32_e32 v11, 16, v0
	v_cmp_ne_u32_e64 s[12:13], 0, v11
	s_xor_b64 s[14:15], s[10:11], s[12:13]
	s_waitcnt lgkmcnt(1)
	v_max_i32_e32 v14, v10, v12
	v_min_i32_e32 v10, v10, v12
	v_cndmask_b32_e64 v10, v10, v14, s[14:15]
	ds_bpermute_b32 v12, v5, v13
	s_waitcnt lgkmcnt(1)
	v_max_i32_e32 v14, v6, v15
	v_min_i32_e32 v6, v6, v15
	v_cndmask_b32_e64 v6, v6, v14, s[14:15]
	ds_bpermute_b32 v14, v5, v9
	s_waitcnt lgkmcnt(1)
	v_max_i32_e32 v15, v13, v12
	v_min_i32_e32 v12, v13, v12
	ds_bpermute_b32 v13, v4, v10
	v_cndmask_b32_e64 v12, v12, v15, s[14:15]
	s_waitcnt lgkmcnt(1)
	v_max_i32_e32 v15, v9, v14
	v_min_i32_e32 v9, v9, v14
	v_cndmask_b32_e64 v9, v9, v15, s[14:15]
	ds_bpermute_b32 v15, v4, v6
	s_waitcnt lgkmcnt(1)
	v_max_i32_e32 v14, v10, v13
	v_min_i32_e32 v10, v10, v13
	s_xor_b64 s[14:15], s[8:9], s[12:13]
	v_cndmask_b32_e64 v10, v10, v14, s[14:15]
	ds_bpermute_b32 v13, v4, v12
	s_waitcnt lgkmcnt(1)
	v_max_i32_e32 v14, v6, v15
	v_min_i32_e32 v6, v6, v15
	v_cndmask_b32_e64 v6, v6, v14, s[14:15]
	ds_bpermute_b32 v14, v4, v9
	s_waitcnt lgkmcnt(1)
	v_max_i32_e32 v15, v12, v13
	v_min_i32_e32 v12, v12, v13
	ds_bpermute_b32 v13, v3, v10
	v_cndmask_b32_e64 v12, v12, v15, s[14:15]
	s_waitcnt lgkmcnt(1)
	v_max_i32_e32 v15, v9, v14
	v_min_i32_e32 v9, v9, v14
	v_cndmask_b32_e64 v9, v9, v15, s[14:15]
	ds_bpermute_b32 v15, v3, v6
	s_waitcnt lgkmcnt(1)
	v_max_i32_e32 v14, v10, v13
	v_min_i32_e32 v10, v10, v13
	s_xor_b64 s[14:15], s[6:7], s[12:13]
	v_cndmask_b32_e64 v10, v10, v14, s[14:15]
	ds_bpermute_b32 v13, v3, v12
	s_waitcnt lgkmcnt(1)
	v_max_i32_e32 v14, v6, v15
	v_min_i32_e32 v6, v6, v15
	v_cndmask_b32_e64 v6, v6, v14, s[14:15]
	ds_bpermute_b32 v14, v3, v9
	s_waitcnt lgkmcnt(1)
	v_max_i32_e32 v15, v12, v13
	v_min_i32_e32 v12, v12, v13
	ds_bpermute_b32 v13, v2, v10
	v_cndmask_b32_e64 v12, v12, v15, s[14:15]
	s_waitcnt lgkmcnt(1)
	v_max_i32_e32 v15, v9, v14
	v_min_i32_e32 v9, v9, v14
	v_cndmask_b32_e64 v9, v9, v15, s[14:15]
	ds_bpermute_b32 v15, v2, v6
	s_waitcnt lgkmcnt(1)
	v_max_i32_e32 v14, v10, v13
	v_min_i32_e32 v10, v10, v13
	s_xor_b64 s[12:13], vcc, s[12:13]
	v_cndmask_b32_e64 v10, v10, v14, s[12:13]
	ds_bpermute_b32 v13, v2, v12
	s_waitcnt lgkmcnt(1)
	v_max_i32_e32 v14, v6, v15
	v_min_i32_e32 v6, v6, v15
	ds_bpermute_b32 v15, v2, v9
	v_cndmask_b32_e64 v6, v6, v14, s[12:13]
	s_waitcnt lgkmcnt(1)
	v_max_i32_e32 v14, v12, v13
	v_min_i32_e32 v12, v12, v13
	v_cndmask_b32_e64 v12, v12, v14, s[12:13]
	s_waitcnt lgkmcnt(0)
	v_max_i32_e32 v13, v9, v15
	v_min_i32_e32 v9, v9, v15
	v_cndmask_b32_e64 v9, v9, v13, s[12:13]
	v_max_i32_e32 v13, v10, v12
	v_min_i32_e32 v10, v10, v12
	v_cmp_eq_u32_e64 s[12:13], 0, v11
	v_max_i32_e32 v12, v6, v9
	v_min_i32_e32 v6, v6, v9
	v_cndmask_b32_e64 v11, v10, v13, s[12:13]
	v_cndmask_b32_e64 v9, v6, v12, s[12:13]
	v_cndmask_b32_e64 v10, v13, v10, s[12:13]
	v_cndmask_b32_e64 v6, v12, v6, s[12:13]
	v_max_i32_e32 v12, v11, v9
	v_min_i32_e32 v9, v11, v9
	v_cndmask_b32_e64 v11, v9, v12, s[12:13]
	v_cndmask_b32_e64 v9, v12, v9, s[12:13]
	v_max_i32_e32 v12, v10, v6
	v_min_i32_e32 v10, v10, v6
	v_xor_b32_e32 v6, 16, v7
	v_cmp_lt_i32_e64 s[14:15], v6, v8
	v_cndmask_b32_e64 v14, v10, v12, s[12:13]
	v_cndmask_b32_e64 v10, v12, v10, s[12:13]
	v_cndmask_b32_e64 v6, v7, v6, s[14:15]
	v_lshlrev_b32_e32 v6, 2, v6
	ds_bpermute_b32 v13, v6, v11
	ds_bpermute_b32 v16, v6, v9
	v_and_b32_e32 v12, 32, v0
	v_cmp_ne_u32_e64 s[14:15], 0, v12
	s_xor_b64 s[16:17], s[12:13], s[14:15]
	s_waitcnt lgkmcnt(1)
	v_max_i32_e32 v15, v11, v13
	v_min_i32_e32 v11, v11, v13
	v_cndmask_b32_e64 v11, v11, v15, s[16:17]
	ds_bpermute_b32 v13, v6, v14
	s_waitcnt lgkmcnt(1)
	v_max_i32_e32 v15, v9, v16
	v_min_i32_e32 v9, v9, v16
	v_cndmask_b32_e64 v9, v9, v15, s[16:17]
	ds_bpermute_b32 v15, v6, v10
	s_waitcnt lgkmcnt(1)
	v_max_i32_e32 v16, v14, v13
	v_min_i32_e32 v13, v14, v13
	ds_bpermute_b32 v14, v5, v11
	v_cndmask_b32_e64 v13, v13, v16, s[16:17]
	s_waitcnt lgkmcnt(1)
	v_max_i32_e32 v16, v10, v15
	v_min_i32_e32 v10, v10, v15
	v_cndmask_b32_e64 v10, v10, v16, s[16:17]
	ds_bpermute_b32 v16, v5, v9
	s_waitcnt lgkmcnt(1)
	v_max_i32_e32 v15, v11, v14
	v_min_i32_e32 v11, v11, v14
	s_xor_b64 s[16:17], s[10:11], s[14:15]
	v_cndmask_b32_e64 v11, v11, v15, s[16:17]
	ds_bpermute_b32 v14, v5, v13
	s_waitcnt lgkmcnt(1)
	v_max_i32_e32 v15, v9, v16
	v_min_i32_e32 v9, v9, v16
	v_cndmask_b32_e64 v9, v9, v15, s[16:17]
	ds_bpermute_b32 v15, v5, v10
	s_waitcnt lgkmcnt(1)
	v_max_i32_e32 v16, v13, v14
	v_min_i32_e32 v13, v13, v14
	ds_bpermute_b32 v14, v4, v11
	v_cndmask_b32_e64 v13, v13, v16, s[16:17]
	s_waitcnt lgkmcnt(1)
	v_max_i32_e32 v16, v10, v15
	v_min_i32_e32 v10, v10, v15
	v_cndmask_b32_e64 v10, v10, v16, s[16:17]
	ds_bpermute_b32 v16, v4, v9
	s_waitcnt lgkmcnt(1)
	v_max_i32_e32 v15, v11, v14
	v_min_i32_e32 v11, v11, v14
	s_xor_b64 s[16:17], s[8:9], s[14:15]
	v_cndmask_b32_e64 v11, v11, v15, s[16:17]
	ds_bpermute_b32 v14, v4, v13
	s_waitcnt lgkmcnt(1)
	v_max_i32_e32 v15, v9, v16
	v_min_i32_e32 v9, v9, v16
	v_cndmask_b32_e64 v9, v9, v15, s[16:17]
	ds_bpermute_b32 v15, v4, v10
	s_waitcnt lgkmcnt(1)
	v_max_i32_e32 v16, v13, v14
	v_min_i32_e32 v13, v13, v14
	ds_bpermute_b32 v14, v3, v11
	v_cndmask_b32_e64 v13, v13, v16, s[16:17]
	s_waitcnt lgkmcnt(1)
	v_max_i32_e32 v16, v10, v15
	v_min_i32_e32 v10, v10, v15
	v_cndmask_b32_e64 v10, v10, v16, s[16:17]
	ds_bpermute_b32 v16, v3, v9
	s_waitcnt lgkmcnt(1)
	v_max_i32_e32 v15, v11, v14
	v_min_i32_e32 v11, v11, v14
	s_xor_b64 s[16:17], s[6:7], s[14:15]
	v_cndmask_b32_e64 v11, v11, v15, s[16:17]
	ds_bpermute_b32 v14, v3, v13
	s_waitcnt lgkmcnt(1)
	v_max_i32_e32 v15, v9, v16
	v_min_i32_e32 v9, v9, v16
	v_cndmask_b32_e64 v9, v9, v15, s[16:17]
	ds_bpermute_b32 v15, v3, v10
	s_waitcnt lgkmcnt(1)
	v_max_i32_e32 v16, v13, v14
	v_min_i32_e32 v13, v13, v14
	ds_bpermute_b32 v14, v2, v11
	v_cndmask_b32_e64 v13, v13, v16, s[16:17]
	s_waitcnt lgkmcnt(1)
	v_max_i32_e32 v16, v10, v15
	v_min_i32_e32 v10, v10, v15
	v_cndmask_b32_e64 v10, v10, v16, s[16:17]
	ds_bpermute_b32 v16, v2, v9
	s_waitcnt lgkmcnt(1)
	v_max_i32_e32 v15, v11, v14
	v_min_i32_e32 v11, v11, v14
	s_xor_b64 s[14:15], vcc, s[14:15]
	v_cndmask_b32_e64 v11, v11, v15, s[14:15]
	ds_bpermute_b32 v14, v2, v13
	s_waitcnt lgkmcnt(1)
	v_max_i32_e32 v15, v9, v16
	v_min_i32_e32 v9, v9, v16
	ds_bpermute_b32 v16, v2, v10
	v_cndmask_b32_e64 v9, v9, v15, s[14:15]
	s_waitcnt lgkmcnt(1)
	v_max_i32_e32 v15, v13, v14
	v_min_i32_e32 v13, v13, v14
	v_cndmask_b32_e64 v13, v13, v15, s[14:15]
	s_waitcnt lgkmcnt(0)
	v_max_i32_e32 v14, v10, v16
	v_min_i32_e32 v10, v10, v16
	v_cndmask_b32_e64 v10, v10, v14, s[14:15]
	v_max_i32_e32 v14, v11, v13
	v_min_i32_e32 v11, v11, v13
	v_cmp_eq_u32_e64 s[14:15], 0, v12
	v_max_i32_e32 v13, v9, v10
	v_min_i32_e32 v9, v9, v10
	v_cndmask_b32_e64 v12, v11, v14, s[14:15]
	v_cndmask_b32_e64 v10, v9, v13, s[14:15]
	v_cndmask_b32_e64 v11, v14, v11, s[14:15]
	v_cndmask_b32_e64 v9, v13, v9, s[14:15]
	v_max_i32_e32 v13, v12, v10
	v_min_i32_e32 v10, v12, v10
	v_cndmask_b32_e64 v12, v10, v13, s[14:15]
	v_cndmask_b32_e64 v10, v13, v10, s[14:15]
	v_max_i32_e32 v13, v11, v9
	v_min_i32_e32 v9, v11, v9
	v_xor_b32_e32 v11, 32, v7
	v_cmp_lt_i32_e64 s[16:17], v11, v8
	v_mov_b32_e32 v251, v197
	s_mov_b32 s31, 0
	v_cndmask_b32_e64 v7, v7, v11, s[16:17]
	v_lshlrev_b32_e32 v7, 2, v7
	ds_bpermute_b32 v8, v7, v12
	ds_bpermute_b32 v15, v7, v10
	v_cndmask_b32_e64 v11, v9, v13, s[14:15]
	v_cndmask_b32_e64 v9, v13, v9, s[14:15]
	v_and_b32_e32 v13, 64, v0
	v_cmp_ne_u32_e64 s[16:17], 0, v13
	s_waitcnt lgkmcnt(1)
	v_max_i32_e32 v14, v12, v8
	v_min_i32_e32 v8, v12, v8
	s_xor_b64 s[18:19], s[14:15], s[16:17]
	v_cndmask_b32_e64 v8, v8, v14, s[18:19]
	ds_bpermute_b32 v12, v7, v11
	s_waitcnt lgkmcnt(1)
	v_max_i32_e32 v14, v10, v15
	v_min_i32_e32 v10, v10, v15
	v_cndmask_b32_e64 v10, v10, v14, s[18:19]
	ds_bpermute_b32 v14, v7, v9
	s_waitcnt lgkmcnt(1)
	v_max_i32_e32 v15, v11, v12
	v_min_i32_e32 v11, v11, v12
	ds_bpermute_b32 v12, v6, v8
	v_cndmask_b32_e64 v11, v11, v15, s[18:19]
	s_waitcnt lgkmcnt(1)
	v_max_i32_e32 v15, v9, v14
	v_min_i32_e32 v9, v9, v14
	v_cndmask_b32_e64 v9, v9, v15, s[18:19]
	ds_bpermute_b32 v15, v6, v10
	s_waitcnt lgkmcnt(1)
	v_max_i32_e32 v14, v8, v12
	v_min_i32_e32 v8, v8, v12
	s_xor_b64 s[18:19], s[12:13], s[16:17]
	v_cndmask_b32_e64 v8, v8, v14, s[18:19]
	ds_bpermute_b32 v12, v6, v11
	s_waitcnt lgkmcnt(1)
	v_max_i32_e32 v14, v10, v15
	v_min_i32_e32 v10, v10, v15
	v_cndmask_b32_e64 v10, v10, v14, s[18:19]
	ds_bpermute_b32 v14, v6, v9
	s_waitcnt lgkmcnt(1)
	v_max_i32_e32 v15, v11, v12
	v_min_i32_e32 v11, v11, v12
	ds_bpermute_b32 v12, v5, v8
	v_cndmask_b32_e64 v11, v11, v15, s[18:19]
	s_waitcnt lgkmcnt(1)
	v_max_i32_e32 v15, v9, v14
	v_min_i32_e32 v9, v9, v14
	v_cndmask_b32_e64 v9, v9, v15, s[18:19]
	ds_bpermute_b32 v15, v5, v10
	s_waitcnt lgkmcnt(1)
	v_max_i32_e32 v14, v8, v12
	v_min_i32_e32 v8, v8, v12
	s_xor_b64 s[18:19], s[10:11], s[16:17]
	v_cndmask_b32_e64 v8, v8, v14, s[18:19]
	ds_bpermute_b32 v12, v5, v11
	s_waitcnt lgkmcnt(1)
	v_max_i32_e32 v14, v10, v15
	v_min_i32_e32 v10, v10, v15
	v_cndmask_b32_e64 v10, v10, v14, s[18:19]
	ds_bpermute_b32 v14, v5, v9
	s_waitcnt lgkmcnt(1)
	v_max_i32_e32 v15, v11, v12
	v_min_i32_e32 v11, v11, v12
	ds_bpermute_b32 v12, v4, v8
	v_cndmask_b32_e64 v11, v11, v15, s[18:19]
	s_waitcnt lgkmcnt(1)
	v_max_i32_e32 v15, v9, v14
	v_min_i32_e32 v9, v9, v14
	v_cndmask_b32_e64 v9, v9, v15, s[18:19]
	ds_bpermute_b32 v15, v4, v10
	s_waitcnt lgkmcnt(1)
	v_max_i32_e32 v14, v8, v12
	v_min_i32_e32 v8, v8, v12
	s_xor_b64 s[18:19], s[8:9], s[16:17]
	v_cndmask_b32_e64 v8, v8, v14, s[18:19]
	ds_bpermute_b32 v12, v4, v11
	s_waitcnt lgkmcnt(1)
	v_max_i32_e32 v14, v10, v15
	v_min_i32_e32 v10, v10, v15
	v_cndmask_b32_e64 v10, v10, v14, s[18:19]
	ds_bpermute_b32 v14, v4, v9
	s_waitcnt lgkmcnt(1)
	v_max_i32_e32 v15, v11, v12
	v_min_i32_e32 v11, v11, v12
	ds_bpermute_b32 v12, v3, v8
	v_cndmask_b32_e64 v11, v11, v15, s[18:19]
	s_waitcnt lgkmcnt(1)
	v_max_i32_e32 v15, v9, v14
	v_min_i32_e32 v9, v9, v14
	v_cndmask_b32_e64 v9, v9, v15, s[18:19]
	ds_bpermute_b32 v15, v3, v10
	s_waitcnt lgkmcnt(1)
	v_max_i32_e32 v14, v8, v12
	v_min_i32_e32 v8, v8, v12
	s_xor_b64 s[18:19], s[6:7], s[16:17]
	v_cndmask_b32_e64 v8, v8, v14, s[18:19]
	ds_bpermute_b32 v12, v3, v11
	s_waitcnt lgkmcnt(1)
	v_max_i32_e32 v14, v10, v15
	v_min_i32_e32 v10, v10, v15
	v_cndmask_b32_e64 v10, v10, v14, s[18:19]
	ds_bpermute_b32 v14, v3, v9
	s_waitcnt lgkmcnt(1)
	v_max_i32_e32 v15, v11, v12
	v_min_i32_e32 v11, v11, v12
	ds_bpermute_b32 v12, v2, v8
	v_cndmask_b32_e64 v11, v11, v15, s[18:19]
	s_waitcnt lgkmcnt(1)
	v_max_i32_e32 v15, v9, v14
	v_min_i32_e32 v9, v9, v14
	v_cndmask_b32_e64 v9, v9, v15, s[18:19]
	ds_bpermute_b32 v15, v2, v10
	s_waitcnt lgkmcnt(1)
	v_max_i32_e32 v14, v8, v12
	v_min_i32_e32 v8, v8, v12
	s_xor_b64 s[16:17], vcc, s[16:17]
	ds_bpermute_b32 v12, v2, v11
	v_cndmask_b32_e64 v8, v8, v14, s[16:17]
	s_waitcnt lgkmcnt(1)
	v_max_i32_e32 v14, v10, v15
	v_min_i32_e32 v10, v10, v15
	ds_bpermute_b32 v15, v2, v9
	v_cndmask_b32_e64 v10, v10, v14, s[16:17]
	s_waitcnt lgkmcnt(1)
	v_max_i32_e32 v14, v11, v12
	v_min_i32_e32 v11, v11, v12
	v_cndmask_b32_e64 v11, v11, v14, s[16:17]
	s_waitcnt lgkmcnt(0)
	v_max_i32_e32 v12, v9, v15
	v_min_i32_e32 v9, v9, v15
	v_cndmask_b32_e64 v9, v9, v12, s[16:17]
	v_max_i32_e32 v12, v8, v11
	v_min_i32_e32 v8, v8, v11
	v_cmp_eq_u32_e64 s[16:17], 0, v13
	v_lshlrev_b32_e32 v208, 11, v82
	v_mov_b32_e32 v209, v197
	v_cndmask_b32_e64 v11, v8, v12, s[16:17]
	v_cndmask_b32_e64 v8, v12, v8, s[16:17]
	v_max_i32_e32 v12, v10, v9
	v_min_i32_e32 v9, v10, v9
	v_cndmask_b32_e64 v10, v9, v12, s[16:17]
	v_cndmask_b32_e64 v9, v12, v9, s[16:17]
	v_max_i32_e32 v13, v11, v10
	v_min_i32_e32 v10, v11, v10
	v_cndmask_b32_e64 v12, v10, v13, s[16:17]
	v_cndmask_b32_e64 v13, v13, v10, s[16:17]
	v_max_i32_e32 v10, v8, v9
	v_min_i32_e32 v8, v8, v9
	v_cndmask_b32_e64 v14, v8, v10, s[16:17]
	v_cndmask_b32_e64 v15, v10, v8, s[16:17]
	ds_write_b128 v1, v[12:15]
	v_xor_b32_e32 v8, 0x100, v252
	s_waitcnt lgkmcnt(0)
	s_barrier
	v_lshl_add_u32 v8, v8, 2, s30
	ds_read_b32 v16, v8
	v_and_b32_e32 v9, 0x80, v0
	v_cmp_ne_u32_e64 s[18:19], 0, v9
	v_xor_b32_e32 v9, 0x101, v252
	v_lshl_add_u32 v9, v9, 2, s30
	v_xor_b32_e32 v10, 0x102, v252
	v_xor_b32_e32 v11, 0x103, v252
	v_lshl_add_u32 v10, v10, 2, s30
	v_lshl_add_u32 v11, v11, 2, s30
	ds_read_b32 v18, v9
	ds_read_b32 v19, v10
	ds_read_b32 v20, v11
	s_waitcnt lgkmcnt(3)
	v_max_i32_e32 v21, v12, v16
	v_min_i32_e32 v12, v12, v16
	s_xor_b64 s[20:21], s[16:17], s[18:19]
	v_cndmask_b32_e64 v12, v12, v21, s[20:21]
	s_waitcnt lgkmcnt(2)
	v_max_i32_e32 v16, v13, v18
	v_min_i32_e32 v13, v13, v18
	v_cndmask_b32_e64 v13, v13, v16, s[20:21]
	ds_bpermute_b32 v18, v7, v12
	s_waitcnt lgkmcnt(2)
	v_max_i32_e32 v16, v14, v19
	v_min_i32_e32 v14, v14, v19
	ds_bpermute_b32 v19, v7, v13
	v_cndmask_b32_e64 v14, v14, v16, s[20:21]
	s_waitcnt lgkmcnt(2)
	v_max_i32_e32 v16, v15, v20
	v_min_i32_e32 v15, v15, v20
	v_cndmask_b32_e64 v15, v15, v16, s[20:21]
	s_waitcnt lgkmcnt(1)
	v_max_i32_e32 v16, v12, v18
	v_min_i32_e32 v12, v12, v18
	s_xor_b64 s[20:21], s[14:15], s[18:19]
	v_cndmask_b32_e64 v12, v12, v16, s[20:21]
	ds_bpermute_b32 v16, v7, v14
	s_waitcnt lgkmcnt(1)
	v_max_i32_e32 v18, v13, v19
	v_min_i32_e32 v13, v13, v19
	v_cndmask_b32_e64 v13, v13, v18, s[20:21]
	ds_bpermute_b32 v18, v7, v15
	s_waitcnt lgkmcnt(1)
	v_max_i32_e32 v19, v14, v16
	v_min_i32_e32 v14, v14, v16
	ds_bpermute_b32 v16, v6, v12
	v_cndmask_b32_e64 v14, v14, v19, s[20:21]
	s_waitcnt lgkmcnt(1)
	v_max_i32_e32 v19, v15, v18
	v_min_i32_e32 v15, v15, v18
	v_cndmask_b32_e64 v15, v15, v19, s[20:21]
	ds_bpermute_b32 v19, v6, v13
	s_waitcnt lgkmcnt(1)
	v_max_i32_e32 v18, v12, v16
	v_min_i32_e32 v12, v12, v16
	s_xor_b64 s[20:21], s[12:13], s[18:19]
	v_cndmask_b32_e64 v12, v12, v18, s[20:21]
	ds_bpermute_b32 v16, v6, v14
	s_waitcnt lgkmcnt(1)
	v_max_i32_e32 v18, v13, v19
	v_min_i32_e32 v13, v13, v19
	v_cndmask_b32_e64 v13, v13, v18, s[20:21]
	ds_bpermute_b32 v18, v6, v15
	s_waitcnt lgkmcnt(1)
	v_max_i32_e32 v19, v14, v16
	v_min_i32_e32 v14, v14, v16
	ds_bpermute_b32 v16, v5, v12
	v_cndmask_b32_e64 v14, v14, v19, s[20:21]
	s_waitcnt lgkmcnt(1)
	v_max_i32_e32 v19, v15, v18
	v_min_i32_e32 v15, v15, v18
	v_cndmask_b32_e64 v15, v15, v19, s[20:21]
	ds_bpermute_b32 v19, v5, v13
	s_waitcnt lgkmcnt(1)
	v_max_i32_e32 v18, v12, v16
	v_min_i32_e32 v12, v12, v16
	s_xor_b64 s[20:21], s[10:11], s[18:19]
	v_cndmask_b32_e64 v12, v12, v18, s[20:21]
	ds_bpermute_b32 v16, v5, v14
	s_waitcnt lgkmcnt(1)
	v_max_i32_e32 v18, v13, v19
	v_min_i32_e32 v13, v13, v19
	v_cndmask_b32_e64 v13, v13, v18, s[20:21]
	ds_bpermute_b32 v18, v5, v15
	s_waitcnt lgkmcnt(1)
	v_max_i32_e32 v19, v14, v16
	v_min_i32_e32 v14, v14, v16
	ds_bpermute_b32 v16, v4, v12
	v_cndmask_b32_e64 v14, v14, v19, s[20:21]
	s_waitcnt lgkmcnt(1)
	v_max_i32_e32 v19, v15, v18
	v_min_i32_e32 v15, v15, v18
	v_cndmask_b32_e64 v15, v15, v19, s[20:21]
	ds_bpermute_b32 v19, v4, v13
	s_waitcnt lgkmcnt(1)
	v_max_i32_e32 v18, v12, v16
	v_min_i32_e32 v12, v12, v16
	s_xor_b64 s[20:21], s[8:9], s[18:19]
	v_cndmask_b32_e64 v12, v12, v18, s[20:21]
	ds_bpermute_b32 v16, v4, v14
	s_waitcnt lgkmcnt(1)
	v_max_i32_e32 v18, v13, v19
	v_min_i32_e32 v13, v13, v19
	v_cndmask_b32_e64 v13, v13, v18, s[20:21]
	ds_bpermute_b32 v18, v4, v15
	s_waitcnt lgkmcnt(1)
	v_max_i32_e32 v19, v14, v16
	v_min_i32_e32 v14, v14, v16
	ds_bpermute_b32 v16, v3, v12
	v_cndmask_b32_e64 v14, v14, v19, s[20:21]
	s_waitcnt lgkmcnt(1)
	v_max_i32_e32 v19, v15, v18
	v_min_i32_e32 v15, v15, v18
	v_cndmask_b32_e64 v15, v15, v19, s[20:21]
	ds_bpermute_b32 v19, v3, v13
	s_waitcnt lgkmcnt(1)
	v_max_i32_e32 v18, v12, v16
	v_min_i32_e32 v12, v12, v16
	s_xor_b64 s[20:21], s[6:7], s[18:19]
	v_cndmask_b32_e64 v12, v12, v18, s[20:21]
	ds_bpermute_b32 v16, v3, v14
	s_waitcnt lgkmcnt(1)
	v_max_i32_e32 v18, v13, v19
	v_min_i32_e32 v13, v13, v19
	v_cndmask_b32_e64 v13, v13, v18, s[20:21]
	ds_bpermute_b32 v18, v3, v15
	s_waitcnt lgkmcnt(1)
	v_max_i32_e32 v19, v14, v16
	v_min_i32_e32 v14, v14, v16
	ds_bpermute_b32 v16, v2, v12
	v_cndmask_b32_e64 v14, v14, v19, s[20:21]
	s_waitcnt lgkmcnt(1)
	v_max_i32_e32 v19, v15, v18
	v_min_i32_e32 v15, v15, v18
	v_cndmask_b32_e64 v15, v15, v19, s[20:21]
	ds_bpermute_b32 v19, v2, v13
	s_waitcnt lgkmcnt(1)
	v_max_i32_e32 v18, v12, v16
	v_min_i32_e32 v12, v12, v16
	s_xor_b64 s[18:19], vcc, s[18:19]
	ds_bpermute_b32 v16, v2, v14
	v_cndmask_b32_e64 v12, v12, v18, s[18:19]
	s_waitcnt lgkmcnt(1)
	v_max_i32_e32 v18, v13, v19
	v_min_i32_e32 v13, v13, v19
	ds_bpermute_b32 v19, v2, v15
	v_cndmask_b32_e64 v13, v13, v18, s[18:19]
	s_waitcnt lgkmcnt(1)
	v_max_i32_e32 v18, v14, v16
	v_min_i32_e32 v14, v14, v16
	v_cndmask_b32_e64 v14, v14, v18, s[18:19]
	s_waitcnt lgkmcnt(0)
	v_max_i32_e32 v16, v15, v19
	v_min_i32_e32 v15, v15, v19
	v_cndmask_b32_e64 v15, v15, v16, s[18:19]
	v_max_i32_e32 v16, v12, v14
	v_min_i32_e32 v12, v12, v14
	v_cmp_eq_u32_e64 s[18:19], 0, v17
	s_waitcnt lgkmcnt(0)
	s_barrier
	v_and_b32_e32 v18, 0x100, v0
	v_cmp_ne_u32_e64 s[20:21], 0, v18
	v_cndmask_b32_e64 v14, v12, v16, s[18:19]
	v_cndmask_b32_e64 v16, v16, v12, s[18:19]
	v_max_i32_e32 v12, v13, v15
	v_min_i32_e32 v13, v13, v15
	v_cndmask_b32_e64 v15, v13, v12, s[18:19]
	v_cndmask_b32_e64 v17, v12, v13, s[18:19]
	v_max_i32_e32 v13, v14, v15
	v_min_i32_e32 v14, v14, v15
	v_max_i32_e32 v15, v16, v17
	v_min_i32_e32 v16, v16, v17
	v_cndmask_b32_e64 v12, v14, v13, s[18:19]
	v_cndmask_b32_e64 v13, v13, v14, s[18:19]
	v_cndmask_b32_e64 v14, v16, v15, s[18:19]
	v_cndmask_b32_e64 v15, v15, v16, s[18:19]
	ds_write_b128 v1, v[12:15]
	v_xor_b32_e32 v16, 0x200, v252
	s_waitcnt lgkmcnt(0)
	s_barrier
	v_lshl_add_u32 v16, v16, 2, s30
	ds_read_b32 v17, v16
	v_xor_b32_e32 v18, 0x201, v252
	v_lshl_add_u32 v18, v18, 2, s30
	v_xor_b32_e32 v19, 0x202, v252
	v_xor_b32_e32 v20, 0x203, v252
	v_lshl_add_u32 v19, v19, 2, s30
	v_lshl_add_u32 v20, v20, 2, s30
	ds_read_b32 v21, v18
	ds_read_b32 v22, v19
	ds_read_b32 v23, v20
	s_waitcnt lgkmcnt(3)
	v_max_i32_e32 v24, v12, v17
	v_min_i32_e32 v12, v12, v17
	s_xor_b64 s[22:23], s[18:19], s[20:21]
	s_waitcnt lgkmcnt(2)
	v_max_i32_e32 v17, v13, v21
	v_min_i32_e32 v13, v13, v21
	v_cndmask_b32_e64 v13, v13, v17, s[22:23]
	s_waitcnt lgkmcnt(1)
	v_max_i32_e32 v17, v14, v22
	v_min_i32_e32 v14, v14, v22
	v_cndmask_b32_e64 v14, v14, v17, s[22:23]
	s_waitcnt lgkmcnt(0)
	v_max_i32_e32 v17, v15, v23
	v_min_i32_e32 v15, v15, v23
	v_cndmask_b32_e64 v12, v12, v24, s[22:23]
	v_cndmask_b32_e64 v15, v15, v17, s[22:23]
	s_waitcnt lgkmcnt(0)
	s_barrier
	ds_write_b128 v1, v[12:15]
	s_waitcnt lgkmcnt(0)
	s_barrier
	ds_read_b32 v17, v8
	ds_read_b32 v22, v9
	ds_read_b32 v23, v10
	ds_read_b32 v24, v11
	s_xor_b64 s[22:23], s[16:17], s[20:21]
	v_and_b32_e32 v21, 0x100, v0
	s_waitcnt lgkmcnt(0)
	s_barrier
	s_waitcnt lgkmcnt(3)
	v_max_i32_e32 v25, v12, v17
	v_min_i32_e32 v12, v12, v17
	v_cndmask_b32_e64 v12, v12, v25, s[22:23]
	s_waitcnt lgkmcnt(2)
	v_max_i32_e32 v17, v13, v22
	v_min_i32_e32 v13, v13, v22
	v_cndmask_b32_e64 v13, v13, v17, s[22:23]
	ds_bpermute_b32 v22, v7, v12
	s_waitcnt lgkmcnt(2)
	v_max_i32_e32 v17, v14, v23
	v_min_i32_e32 v14, v14, v23
	ds_bpermute_b32 v23, v7, v13
	v_cndmask_b32_e64 v14, v14, v17, s[22:23]
	s_waitcnt lgkmcnt(2)
	v_max_i32_e32 v17, v15, v24
	v_min_i32_e32 v15, v15, v24
	v_cndmask_b32_e64 v15, v15, v17, s[22:23]
	s_waitcnt lgkmcnt(1)
	v_max_i32_e32 v17, v12, v22
	v_min_i32_e32 v12, v12, v22
	s_xor_b64 s[22:23], s[14:15], s[20:21]
	v_cndmask_b32_e64 v12, v12, v17, s[22:23]
	ds_bpermute_b32 v17, v7, v14
	s_waitcnt lgkmcnt(1)
	v_max_i32_e32 v22, v13, v23
	v_min_i32_e32 v13, v13, v23
	v_cndmask_b32_e64 v13, v13, v22, s[22:23]
	ds_bpermute_b32 v22, v7, v15
	s_waitcnt lgkmcnt(1)
	v_max_i32_e32 v23, v14, v17
	v_min_i32_e32 v14, v14, v17
	ds_bpermute_b32 v17, v6, v12
	v_cndmask_b32_e64 v14, v14, v23, s[22:23]
	s_waitcnt lgkmcnt(1)
	v_max_i32_e32 v23, v15, v22
	v_min_i32_e32 v15, v15, v22
	v_cndmask_b32_e64 v15, v15, v23, s[22:23]
	ds_bpermute_b32 v23, v6, v13
	s_waitcnt lgkmcnt(1)
	v_max_i32_e32 v22, v12, v17
	v_min_i32_e32 v12, v12, v17
	s_xor_b64 s[22:23], s[12:13], s[20:21]
	v_cndmask_b32_e64 v12, v12, v22, s[22:23]
	ds_bpermute_b32 v17, v6, v14
	s_waitcnt lgkmcnt(1)
	v_max_i32_e32 v22, v13, v23
	v_min_i32_e32 v13, v13, v23
	v_cndmask_b32_e64 v13, v13, v22, s[22:23]
	ds_bpermute_b32 v22, v6, v15
	s_waitcnt lgkmcnt(1)
	v_max_i32_e32 v23, v14, v17
	v_min_i32_e32 v14, v14, v17
	ds_bpermute_b32 v17, v5, v12
	v_cndmask_b32_e64 v14, v14, v23, s[22:23]
	s_waitcnt lgkmcnt(1)
	v_max_i32_e32 v23, v15, v22
	v_min_i32_e32 v15, v15, v22
	v_cndmask_b32_e64 v15, v15, v23, s[22:23]
	ds_bpermute_b32 v23, v5, v13
	s_waitcnt lgkmcnt(1)
	v_max_i32_e32 v22, v12, v17
	v_min_i32_e32 v12, v12, v17
	s_xor_b64 s[22:23], s[10:11], s[20:21]
	v_cndmask_b32_e64 v12, v12, v22, s[22:23]
	ds_bpermute_b32 v17, v5, v14
	s_waitcnt lgkmcnt(1)
	v_max_i32_e32 v22, v13, v23
	v_min_i32_e32 v13, v13, v23
	v_cndmask_b32_e64 v13, v13, v22, s[22:23]
	ds_bpermute_b32 v22, v5, v15
	s_waitcnt lgkmcnt(1)
	v_max_i32_e32 v23, v14, v17
	v_min_i32_e32 v14, v14, v17
	ds_bpermute_b32 v17, v4, v12
	v_cndmask_b32_e64 v14, v14, v23, s[22:23]
	s_waitcnt lgkmcnt(1)
	v_max_i32_e32 v23, v15, v22
	v_min_i32_e32 v15, v15, v22
	v_cndmask_b32_e64 v15, v15, v23, s[22:23]
	ds_bpermute_b32 v23, v4, v13
	s_waitcnt lgkmcnt(1)
	v_max_i32_e32 v22, v12, v17
	v_min_i32_e32 v12, v12, v17
	s_xor_b64 s[22:23], s[8:9], s[20:21]
	v_cndmask_b32_e64 v12, v12, v22, s[22:23]
	ds_bpermute_b32 v17, v4, v14
	s_waitcnt lgkmcnt(1)
	v_max_i32_e32 v22, v13, v23
	v_min_i32_e32 v13, v13, v23
	v_cndmask_b32_e64 v13, v13, v22, s[22:23]
	ds_bpermute_b32 v22, v4, v15
	s_waitcnt lgkmcnt(1)
	v_max_i32_e32 v23, v14, v17
	v_min_i32_e32 v14, v14, v17
	ds_bpermute_b32 v17, v3, v12
	v_cndmask_b32_e64 v14, v14, v23, s[22:23]
	s_waitcnt lgkmcnt(1)
	v_max_i32_e32 v23, v15, v22
	v_min_i32_e32 v15, v15, v22
	v_cndmask_b32_e64 v15, v15, v23, s[22:23]
	ds_bpermute_b32 v23, v3, v13
	s_waitcnt lgkmcnt(1)
	v_max_i32_e32 v22, v12, v17
	v_min_i32_e32 v12, v12, v17
	s_xor_b64 s[22:23], s[6:7], s[20:21]
	v_cndmask_b32_e64 v12, v12, v22, s[22:23]
	ds_bpermute_b32 v17, v3, v14
	s_waitcnt lgkmcnt(1)
	v_max_i32_e32 v22, v13, v23
	v_min_i32_e32 v13, v13, v23
	v_cndmask_b32_e64 v13, v13, v22, s[22:23]
	ds_bpermute_b32 v22, v3, v15
	s_waitcnt lgkmcnt(1)
	v_max_i32_e32 v23, v14, v17
	v_min_i32_e32 v14, v14, v17
	ds_bpermute_b32 v17, v2, v12
	v_cndmask_b32_e64 v14, v14, v23, s[22:23]
	s_waitcnt lgkmcnt(1)
	v_max_i32_e32 v23, v15, v22
	v_min_i32_e32 v15, v15, v22
	v_cndmask_b32_e64 v15, v15, v23, s[22:23]
	ds_bpermute_b32 v23, v2, v13
	s_waitcnt lgkmcnt(1)
	v_max_i32_e32 v22, v12, v17
	v_min_i32_e32 v12, v12, v17
	s_xor_b64 s[20:21], vcc, s[20:21]
	ds_bpermute_b32 v17, v2, v14
	v_cndmask_b32_e64 v12, v12, v22, s[20:21]
	s_waitcnt lgkmcnt(1)
	v_max_i32_e32 v22, v13, v23
	v_min_i32_e32 v13, v13, v23
	ds_bpermute_b32 v23, v2, v15
	v_cndmask_b32_e64 v13, v13, v22, s[20:21]
	s_waitcnt lgkmcnt(1)
	v_max_i32_e32 v22, v14, v17
	v_min_i32_e32 v14, v14, v17
	v_cndmask_b32_e64 v14, v14, v22, s[20:21]
	s_waitcnt lgkmcnt(0)
	v_max_i32_e32 v17, v15, v23
	v_min_i32_e32 v15, v15, v23
	v_cndmask_b32_e64 v15, v15, v17, s[20:21]
	v_max_i32_e32 v17, v12, v14
	v_min_i32_e32 v12, v12, v14
	v_cmp_eq_u32_e64 s[22:23], 0, v21
	v_xor_b32_e32 v22, 0x402, v252
	v_xor_b32_e32 v23, 0x403, v252
	v_cndmask_b32_e64 v14, v12, v17, s[22:23]
	v_cndmask_b32_e64 v17, v17, v12, s[22:23]
	v_max_i32_e32 v12, v13, v15
	v_min_i32_e32 v13, v13, v15
	v_cndmask_b32_e64 v15, v13, v12, s[22:23]
	v_cndmask_b32_e64 v21, v12, v13, s[22:23]
	v_max_i32_e32 v13, v14, v15
	v_min_i32_e32 v14, v14, v15
	v_max_i32_e32 v15, v17, v21
	v_min_i32_e32 v17, v17, v21
	v_cndmask_b32_e64 v12, v14, v13, s[22:23]
	v_cndmask_b32_e64 v13, v13, v14, s[22:23]
	v_cndmask_b32_e64 v14, v17, v15, s[22:23]
	v_cndmask_b32_e64 v15, v15, v17, s[22:23]
	ds_write_b128 v1, v[12:15]
	v_xor_b32_e32 v17, 0x400, v252
	s_waitcnt lgkmcnt(0)
	s_barrier
	v_lshl_add_u32 v17, v17, 2, s30
	ds_read_b32 v17, v17
	v_xor_b32_e32 v21, 0x401, v252
	v_lshl_add_u32 v21, v21, 2, s30
	v_lshl_add_u32 v22, v22, 2, s30
	v_lshl_add_u32 v23, v23, 2, s30
	ds_read_b32 v21, v21
	ds_read_b32 v22, v22
	ds_read_b32 v23, v23
	s_movk_i32 s20, 0x1ff
	v_cmp_lt_u32_e64 s[20:21], s20, v0
	s_waitcnt lgkmcnt(3)
	v_max_i32_e32 v24, v12, v17
	v_min_i32_e32 v12, v12, v17
	s_xor_b64 s[22:23], s[22:23], s[20:21]
	s_waitcnt lgkmcnt(2)
	v_max_i32_e32 v17, v13, v21
	v_min_i32_e32 v13, v13, v21
	v_cndmask_b32_e64 v13, v13, v17, s[22:23]
	s_waitcnt lgkmcnt(1)
	v_max_i32_e32 v17, v14, v22
	v_min_i32_e32 v14, v14, v22
	v_cndmask_b32_e64 v14, v14, v17, s[22:23]
	s_waitcnt lgkmcnt(0)
	v_max_i32_e32 v17, v15, v23
	v_min_i32_e32 v15, v15, v23
	v_cndmask_b32_e64 v12, v12, v24, s[22:23]
	v_cndmask_b32_e64 v15, v15, v17, s[22:23]
	s_waitcnt lgkmcnt(0)
	s_barrier
	ds_write_b128 v1, v[12:15]
	s_waitcnt lgkmcnt(0)
	s_barrier
	ds_read_b32 v16, v16
	ds_read_b32 v17, v18
	ds_read_b32 v18, v19
	ds_read_b32 v19, v20
	s_xor_b64 s[18:19], s[18:19], s[20:21]
	s_waitcnt lgkmcnt(0)
	s_barrier
	s_xor_b64 s[16:17], s[16:17], s[20:21]
	s_waitcnt lgkmcnt(3)
	v_max_i32_e32 v20, v12, v16
	v_min_i32_e32 v12, v12, v16
	s_waitcnt lgkmcnt(2)
	v_max_i32_e32 v16, v13, v17
	v_min_i32_e32 v13, v13, v17
	v_cndmask_b32_e64 v13, v13, v16, s[18:19]
	s_waitcnt lgkmcnt(1)
	v_max_i32_e32 v16, v14, v18
	v_min_i32_e32 v14, v14, v18
	v_cndmask_b32_e64 v14, v14, v16, s[18:19]
	s_waitcnt lgkmcnt(0)
	v_max_i32_e32 v16, v15, v19
	v_min_i32_e32 v15, v15, v19
	v_cndmask_b32_e64 v12, v12, v20, s[18:19]
	v_cndmask_b32_e64 v15, v15, v16, s[18:19]
	ds_write_b128 v1, v[12:15]
	s_waitcnt lgkmcnt(0)
	s_barrier
	ds_read_b32 v8, v8
	ds_read_b32 v9, v9
	ds_read_b32 v10, v10
	ds_read_b32 v11, v11
	s_xor_b64 s[14:15], s[14:15], s[20:21]
	s_xor_b64 s[12:13], s[12:13], s[20:21]
	s_xor_b64 s[10:11], s[10:11], s[20:21]
	s_waitcnt lgkmcnt(3)
	v_max_i32_e32 v16, v12, v8
	v_min_i32_e32 v8, v12, v8
	v_cndmask_b32_e64 v8, v8, v16, s[16:17]
	s_waitcnt lgkmcnt(2)
	v_max_i32_e32 v12, v13, v9
	v_min_i32_e32 v9, v13, v9
	ds_bpermute_b32 v13, v7, v8
	v_cndmask_b32_e64 v9, v9, v12, s[16:17]
	s_waitcnt lgkmcnt(2)
	v_max_i32_e32 v12, v14, v10
	v_min_i32_e32 v10, v14, v10
	v_cndmask_b32_e64 v10, v10, v12, s[16:17]
	s_waitcnt lgkmcnt(1)
	v_max_i32_e32 v12, v15, v11
	v_min_i32_e32 v11, v15, v11
	v_cndmask_b32_e64 v11, v11, v12, s[16:17]
	s_waitcnt lgkmcnt(0)
	v_max_i32_e32 v12, v8, v13
	ds_bpermute_b32 v14, v7, v9
	v_min_i32_e32 v8, v8, v13
	v_cndmask_b32_e64 v8, v8, v12, s[14:15]
	ds_bpermute_b32 v12, v7, v10
	ds_bpermute_b32 v7, v7, v11
	s_waitcnt lgkmcnt(2)
	v_max_i32_e32 v13, v9, v14
	v_min_i32_e32 v9, v9, v14
	v_cndmask_b32_e64 v9, v9, v13, s[14:15]
	s_waitcnt lgkmcnt(1)
	v_max_i32_e32 v13, v10, v12
	v_min_i32_e32 v10, v10, v12
	ds_bpermute_b32 v12, v6, v8
	v_cndmask_b32_e64 v10, v10, v13, s[14:15]
	s_waitcnt lgkmcnt(1)
	v_max_i32_e32 v13, v11, v7
	v_min_i32_e32 v7, v11, v7
	v_cndmask_b32_e64 v7, v7, v13, s[14:15]
	s_waitcnt lgkmcnt(0)
	v_max_i32_e32 v11, v8, v12
	ds_bpermute_b32 v13, v6, v9
	v_min_i32_e32 v8, v8, v12
	v_cndmask_b32_e64 v8, v8, v11, s[12:13]
	ds_bpermute_b32 v11, v6, v10
	ds_bpermute_b32 v6, v6, v7
	s_waitcnt lgkmcnt(2)
	v_max_i32_e32 v12, v9, v13
	v_min_i32_e32 v9, v9, v13
	v_cndmask_b32_e64 v9, v9, v12, s[12:13]
	s_waitcnt lgkmcnt(1)
	v_max_i32_e32 v12, v10, v11
	v_min_i32_e32 v10, v10, v11
	ds_bpermute_b32 v11, v5, v8
	v_cndmask_b32_e64 v10, v10, v12, s[12:13]
	s_waitcnt lgkmcnt(1)
	v_max_i32_e32 v12, v7, v6
	v_min_i32_e32 v6, v7, v6
	v_cndmask_b32_e64 v6, v6, v12, s[12:13]
	s_waitcnt lgkmcnt(0)
	v_max_i32_e32 v7, v8, v11
	ds_bpermute_b32 v12, v5, v9
	v_min_i32_e32 v8, v8, v11
	v_cndmask_b32_e64 v7, v8, v7, s[10:11]
	ds_bpermute_b32 v8, v5, v10
	ds_bpermute_b32 v5, v5, v6
	s_waitcnt lgkmcnt(2)
	v_max_i32_e32 v11, v9, v12
	v_min_i32_e32 v9, v9, v12
	v_cndmask_b32_e64 v9, v9, v11, s[10:11]
	s_waitcnt lgkmcnt(1)
	v_max_i32_e32 v11, v10, v8
	v_min_i32_e32 v8, v10, v8
	ds_bpermute_b32 v10, v4, v7
	v_cndmask_b32_e64 v8, v8, v11, s[10:11]
	s_waitcnt lgkmcnt(1)
	v_max_i32_e32 v11, v6, v5
	v_min_i32_e32 v5, v6, v5
	v_cndmask_b32_e64 v5, v5, v11, s[10:11]
	s_waitcnt lgkmcnt(0)
	v_max_i32_e32 v6, v7, v10
	ds_bpermute_b32 v11, v4, v9
	v_min_i32_e32 v7, v7, v10
	s_xor_b64 s[8:9], s[8:9], s[20:21]
	v_cndmask_b32_e64 v6, v7, v6, s[8:9]
	ds_bpermute_b32 v7, v4, v8
	s_waitcnt lgkmcnt(1)
	v_max_i32_e32 v10, v9, v11
	v_min_i32_e32 v9, v9, v11
	ds_bpermute_b32 v4, v4, v5
	v_cndmask_b32_e64 v9, v9, v10, s[8:9]
	s_waitcnt lgkmcnt(1)
	v_max_i32_e32 v10, v8, v7
	v_min_i32_e32 v7, v8, v7
	ds_bpermute_b32 v8, v3, v6
	v_cndmask_b32_e64 v7, v7, v10, s[8:9]
	s_waitcnt lgkmcnt(1)
	v_max_i32_e32 v10, v5, v4
	v_min_i32_e32 v4, v5, v4
	v_cndmask_b32_e64 v4, v4, v10, s[8:9]
	s_waitcnt lgkmcnt(0)
	v_max_i32_e32 v5, v6, v8
	ds_bpermute_b32 v10, v3, v9
	v_min_i32_e32 v6, v6, v8
	s_xor_b64 s[6:7], s[6:7], s[20:21]
	v_cndmask_b32_e64 v5, v6, v5, s[6:7]
	ds_bpermute_b32 v6, v3, v7
	s_waitcnt lgkmcnt(1)
	v_max_i32_e32 v8, v9, v10
	v_min_i32_e32 v9, v9, v10
	ds_bpermute_b32 v3, v3, v4
	v_cndmask_b32_e64 v8, v9, v8, s[6:7]
	s_waitcnt lgkmcnt(1)
	v_max_i32_e32 v9, v7, v6
	v_min_i32_e32 v6, v7, v6
	ds_bpermute_b32 v7, v2, v5
	v_cndmask_b32_e64 v6, v6, v9, s[6:7]
	s_waitcnt lgkmcnt(1)
	v_max_i32_e32 v9, v4, v3
	v_min_i32_e32 v3, v4, v3
	v_cndmask_b32_e64 v3, v3, v9, s[6:7]
	s_waitcnt lgkmcnt(0)
	v_max_i32_e32 v4, v5, v7
	ds_bpermute_b32 v9, v2, v8
	v_min_i32_e32 v5, v5, v7
	s_xor_b64 vcc, vcc, s[20:21]
	v_cndmask_b32_e32 v4, v5, v4, vcc
	ds_bpermute_b32 v5, v2, v6
	ds_bpermute_b32 v2, v2, v3
	s_waitcnt lgkmcnt(2)
	v_max_i32_e32 v7, v8, v9
	v_min_i32_e32 v8, v8, v9
	v_cndmask_b32_e32 v7, v8, v7, vcc
	s_waitcnt lgkmcnt(1)
	v_max_i32_e32 v8, v6, v5
	v_min_i32_e32 v5, v6, v5
	s_movk_i32 s18, 0x200
	v_cndmask_b32_e32 v5, v5, v8, vcc
	s_waitcnt lgkmcnt(0)
	v_max_i32_e32 v6, v3, v2
	v_min_i32_e32 v2, v3, v2
	v_cndmask_b32_e32 v2, v2, v6, vcc
	v_max_i32_e32 v3, v4, v5
	v_min_i32_e32 v4, v4, v5
	v_cmp_gt_u32_e32 vcc, s18, v0
	s_add_i32 s8, 0, 0x20100
	s_cmp_lg_u32 0, -1
	v_cndmask_b32_e32 v5, v4, v3, vcc
	v_cndmask_b32_e32 v4, v3, v4, vcc
	v_max_i32_e32 v3, v7, v2
	v_min_i32_e32 v2, v7, v2
	v_cndmask_b32_e32 v6, v2, v3, vcc
	v_cndmask_b32_e32 v7, v3, v2, vcc
	v_max_i32_e32 v3, v5, v6
	v_min_i32_e32 v5, v5, v6
	v_cndmask_b32_e32 v2, v5, v3, vcc
	v_cndmask_b32_e32 v3, v3, v5, vcc
	v_max_i32_e32 v5, v4, v7
	v_min_i32_e32 v6, v4, v7
	v_cndmask_b32_e32 v4, v6, v5, vcc
	v_cndmask_b32_e32 v5, v5, v6, vcc
	s_waitcnt lgkmcnt(0)
	s_barrier
	ds_write_b128 v1, v[2:5]
	v_lshl_add_u32 v230, v0, 2, s8
	v_lshrrev_b32_e32 v3, 5, v82
	s_cselect_b32 s8, 0, 0
	v_and_b32_e32 v1, 32, v193
	s_addk_i32 s8, 0x6000
	v_lshlrev_b32_e32 v231, 2, v3
	v_lshrrev_b32_e32 v4, 2, v0
	v_add_u32_e32 v5, s8, v1
	v_and_or_b32 v4, v4, 3, v231
	v_add_u32_e32 v9, 0, v1
	v_lshlrev_b32_e32 v1, 10, v205
	s_movk_i32 s22, 0x100
	v_and_b32_e32 v2, 24, v158
	v_lshlrev_b32_e32 v6, 6, v4
	v_lshlrev_b32_e32 v7, 10, v3
	v_lshl_or_b32 v4, v3, 3, v1
	s_add_i32 s8, 0, 0x15000
	v_lshlrev_b32_e32 v1, 4, v3
	v_lshlrev_b32_e32 v207, 9, v3
	v_lshrrev_b32_e32 v3, 3, v82
	v_cmp_gt_u32_e64 s[6:7], s22, v0
	v_add_u32_e32 v233, s8, v1
	v_add3_u32 v234, v5, v2, v6
	v_or_b32_e32 v5, 8, v3
	v_add_u32_e32 v236, s8, v250
	v_readlane_b32 s8, v253, 46
	v_lshlrev_b32_e32 v8, 4, v205
	v_lshlrev_b32_e32 v195, 7, v3
	v_lshlrev_b32_e32 v200, 10, v3
	v_lshlrev_b32_e32 v199, 7, v5
	v_lshlrev_b32_e32 v202, 10, v5
	v_or_b32_e32 v5, 16, v3
	v_or_b32_e32 v3, 24, v3
	v_readlane_b32 s9, v253, 47
	v_readlane_b32 s20, v253, 58
	v_readlane_b32 s21, v253, 59
	v_readlane_b32 s22, v253, 60
	v_readlane_b32 s23, v253, 61
	v_add3_u32 v232, 0, v7, v8
	v_add3_u32 v235, v9, v2, v6
	v_lshlrev_b32_e32 v203, 7, v3
	v_lshlrev_b32_e32 v206, 10, v3
	v_readlane_b32 s10, v253, 48
	v_readlane_b32 s11, v253, 49
	v_readlane_b32 s12, v253, 50
	v_readlane_b32 s13, v253, 51
	v_readlane_b32 s14, v253, 52
	v_readlane_b32 s15, v253, 53
	v_readlane_b32 s16, v253, 54
	v_readlane_b32 s17, v253, 55
	v_readlane_b32 s18, v253, 56
	v_readlane_b32 s19, v253, 57
	v_lshl_add_u64 v[6:7], s[22:23], 0, v[250:251]
	s_mov_b64 s[8:9], 0x1480000
	v_add_u32_e32 v3, 0, v1
	s_mov_b32 s20, 0xfffe0000
	v_and_b32_e32 v198, 56, v158
	v_lshlrev_b32_e32 v201, 7, v5
	v_lshlrev_b32_e32 v204, 10, v5
	v_lshl_add_u64 v[210:211], v[6:7], 0, s[8:9]
	v_add_u32_e32 v241, 0x15100, v3
	v_or_b32_e32 v237, 0x17b, v231
	s_mov_b64 s[10:11], 0x2000
	v_lshlrev_b32_e32 v212, 1, v2
	s_mov_b64 s[12:13], 0x20000
	v_lshlrev_b32_e32 v238, 1, v4
	s_mov_b64 s[14:15], 0x40000
	s_mov_b64 s[16:17], 0x60000
	s_mov_b64 s[18:19], 0xa0000
	s_mov_b32 s21, -1
	s_mov_b64 s[22:23], 0x80000
	s_movk_i32 s46, 0x1000
	v_mov_b32_e32 v239, 0x7f800000
	v_mov_b32_e32 v240, 0xff800000
	s_mov_b32 s47, 0
	s_cmp_lg_u32 s92, 0
	s_cbranch_scc1 .Lgw_end_9
	s_mov_b64 exec, 1
	v_mov_b32_e32 v2, 0x22160
	ds_read_b32 v246, v2
	s_lshr_b32 s8, s99, 16
	s_add_u32 s8, s100, s8
	s_addc_u32 s9, s101, 0
	s_min_u32 s30, s98, 32
	v_mov_b32_e32 v2, 0
	v_mov_b32_e32 v247, 0
	s_waitcnt lgkmcnt(0)
	v_readfirstlane_b32 vcc_lo, v246
	s_mul_i32 s30, s30, vcc_lo

.LBB0_1750:
	s_waitcnt vmcnt(0)
	s_waitcnt lgkmcnt(0)
	s_barrier
	s_mov_b64 s[6:7], exec
	v_readlane_b32 s40, v253, 46
	s_and_b64 s[8:9], s[6:7], s[78:79]
	v_readlane_b32 s41, v253, 47
	v_readlane_b32 s42, v253, 48
	v_readlane_b32 s43, v253, 49
	v_readlane_b32 s44, v253, 50
	v_readlane_b32 s45, v253, 51
	v_readlane_b32 s52, v253, 58
	v_readlane_b32 s53, v253, 59
	v_readlane_b32 s54, v253, 60
	v_readlane_b32 s55, v253, 61
	v_and_b32_e32 v82, 63, v0
	v_readlane_b32 s46, v253, 52
	v_readlane_b32 s47, v253, 53
	v_readlane_b32 s48, v253, 54
	v_readlane_b32 s49, v253, 55
	v_readlane_b32 s50, v253, 56
	v_readlane_b32 s51, v253, 57
	s_mov_b64 exec, s[8:9]
	s_cbranch_execz .LBB0_1802
	v_mov_b32_e32 v2, 0x22160
	s_waitcnt vmcnt(0) lgkmcnt(0)
	ds_read_b32 v3, v2
	v_mov_b32_e32 v4, 1
	v_mov_b32_e32 v5, s99
	v_and_b32_e32 v6, 0xffff, v5
	v_lshrrev_b32_e32 v7, 16, v5
	global_atomic_add v8, v6, v4, s[100:101] sc0
	buffer_inv sc1
	v_lshrrev_b32_e32 v9, 7, v6
	v_sub_u32_e32 v9, s98, v9
	v_add_u32_e32 v9, 31, v9
	v_lshrrev_b32_e32 v9, 5, v9
	v_mov_b32_e32 v10, s98
	v_min_u32_e32 v10, 32, v10
	v_mov_b32_e32 v11, 0
	s_waitcnt lgkmcnt(0)
	v_add_u32_e32 v3, 1, v3
	ds_write_b32 v2, v3
	v_mul_lo_u32 v9, v9, v3
	v_mul_lo_u32 v10, v10, v3
	s_waitcnt vmcnt(0)
	v_add_u32_e32 v8, 1, v8
	v_cmp_eq_u32_e32 vcc, v8, v9
	s_cbranch_vccz .Lgb_poll_10
	s_mov_b64 exec, -1
	v_mbcnt_lo_u32_b32 v5, -1, 0
	v_mbcnt_hi_u32_b32 v5, -1, v5
	v_lshlrev_b32_e32 v5, 7, v5
	v_add_u32_e32 v5, 0x1000, v5
	v_mov_b32_e32 v4, 1
	global_atomic_add v5, v4, s[100:101]
	s_mov_b64 exec, 1

.LBB0_1811:
	s_cmp_gt_i32 s81, 11
	s_cselect_b64 s[4:5], -1, 0
	s_and_b64 s[0:1], s[0:1], s[4:5]
	v_readlane_b32 s36, v253, 46
	s_andn2_b64 vcc, exec, s[0:1]
	v_readlane_b32 s37, v253, 47
	v_readlane_b32 s38, v253, 48
	v_readlane_b32 s39, v253, 49
	v_readlane_b32 s40, v253, 50
	v_readlane_b32 s41, v253, 51
	v_readlane_b32 s48, v253, 58
	v_readlane_b32 s49, v253, 59
	v_readlane_b32 s50, v253, 60
	v_readlane_b32 s51, v253, 61
	v_readlane_b32 s42, v253, 52
	v_readlane_b32 s43, v253, 53
	v_readlane_b32 s44, v253, 54
	v_readlane_b32 s45, v253, 55
	v_readlane_b32 s46, v253, 56
	v_readlane_b32 s47, v253, 57
	s_cbranch_vccnz .LBB0_1865
	s_waitcnt vmcnt(0)
	s_waitcnt lgkmcnt(0)
	s_barrier
	s_and_saveexec_b64 s[0:1], s[78:79]
	s_cbranch_execz .LBB0_1864
	v_mov_b32_e32 v1, 0x22160
	s_waitcnt vmcnt(0) lgkmcnt(0)
	ds_read_b32 v2, v1
	v_mov_b32_e32 v3, 1
	v_mov_b32_e32 v4, s99
	v_and_b32_e32 v5, 0xffff, v4
	v_lshrrev_b32_e32 v6, 16, v4
	global_atomic_add v7, v5, v3, s[100:101] sc0
	buffer_inv sc1
	v_lshrrev_b32_e32 v8, 7, v5
	v_sub_u32_e32 v8, s98, v8
	v_add_u32_e32 v8, 31, v8
	v_lshrrev_b32_e32 v8, 5, v8
	v_mov_b32_e32 v9, s98
	v_min_u32_e32 v9, 32, v9
	v_mov_b32_e32 v10, 0
	s_waitcnt lgkmcnt(0)
	v_add_u32_e32 v2, 1, v2
	ds_write_b32 v1, v2
	v_mul_lo_u32 v8, v8, v2
	v_mul_lo_u32 v9, v9, v2
	s_waitcnt vmcnt(0)
	v_add_u32_e32 v7, 1, v7
	v_cmp_eq_u32_e32 vcc, v7, v8
	s_cbranch_vccz .Lgb_poll_11
	s_mov_b64 exec, -1
	v_mbcnt_lo_u32_b32 v4, -1, 0
	v_mbcnt_hi_u32_b32 v4, -1, v4
	v_lshlrev_b32_e32 v4, 7, v4
	v_add_u32_e32 v4, 0x1000, v4
	v_mov_b32_e32 v3, 1
	global_atomic_add v4, v3, s[100:101]
	s_mov_b64 exec, 1

.LBB0_1890:
	s_cmp_gt_i32 s81, 12
	s_cselect_b64 s[2:3], -1, 0
	s_and_b64 s[0:1], s[0:1], s[2:3]
	s_andn2_b64 vcc, exec, s[0:1]
	s_cbranch_vccnz .LBB0_1944
	s_waitcnt vmcnt(0)
	s_waitcnt lgkmcnt(0)
	s_barrier
	s_and_saveexec_b64 s[0:1], s[78:79]
	s_cbranch_execz .LBB0_1943
	v_mov_b32_e32 v1, 0x22160
	s_waitcnt vmcnt(0) lgkmcnt(0)
	ds_read_b32 v2, v1
	v_mov_b32_e32 v3, 1
	v_mov_b32_e32 v4, s99
	v_and_b32_e32 v5, 0xffff, v4
	v_lshrrev_b32_e32 v6, 16, v4
	global_atomic_add v7, v5, v3, s[100:101] sc0
	buffer_inv sc1
	v_lshrrev_b32_e32 v8, 7, v5
	v_sub_u32_e32 v8, s98, v8
	v_add_u32_e32 v8, 31, v8
	v_lshrrev_b32_e32 v8, 5, v8
	v_mov_b32_e32 v9, s98
	v_min_u32_e32 v9, 32, v9
	v_mov_b32_e32 v10, 0
	s_waitcnt lgkmcnt(0)
	v_add_u32_e32 v2, 1, v2
	ds_write_b32 v1, v2
	v_mul_lo_u32 v8, v8, v2
	v_mul_lo_u32 v9, v9, v2
	s_waitcnt vmcnt(0)
	v_add_u32_e32 v7, 1, v7
	v_cmp_eq_u32_e32 vcc, v7, v8
	s_cbranch_vccz .Lgb_done_12
	s_mov_b64 exec, -1
	v_mbcnt_lo_u32_b32 v4, -1, 0
	v_mbcnt_hi_u32_b32 v4, -1, v4
	v_lshlrev_b32_e32 v4, 7, v4
	v_add_u32_e32 v4, 0x1000, v4
	v_mov_b32_e32 v3, 1
	global_atomic_add v4, v3, s[100:101]
	s_mov_b64 exec, 1

.LBB0_1953:
	s_or_b64 exec, exec, s[2:3]
	s_lshl_b32 s16, s95, 6
	v_or_b32_e32 v18, s16, v222
	v_ashrrev_i32_e32 v19, 31, v18
	v_lshlrev_b64 v[2:3], 11, v[18:19]
	v_and_b32_e32 v1, 48, v0
	v_lshl_add_u64 v[2:3], s[82:83], 0, v[2:3]
	v_lshl_or_b32 v20, s92, 8, v1
	v_mov_b32_e32 v21, 0
	v_lshl_add_u64 v[24:25], v[2:3], 0, v[20:21]
	s_and_saveexec_b64 s[8:9], s[78:79]
	s_cbranch_execz .Lgw_end_12
	v_mov_b32_e32 v1, 0x22160
	ds_read_b32 v2, v1
	v_mov_b32_e32 v3, s99
	v_lshrrev_b32_e32 v4, 16, v3
	v_mov_b32_e32 v5, s98
	v_min_u32_e32 v5, 32, v5
	v_mov_b32_e32 v6, 0
	s_waitcnt lgkmcnt(0)
	v_mul_lo_u32 v5, v5, v2

.LBB0_1991:
	s_cmp_gt_i32 s81, 13
	s_cselect_b64 s[2:3], -1, 0
	s_and_b64 s[0:1], s[0:1], s[2:3]
	s_andn2_b64 vcc, exec, s[0:1]
	s_cbranch_vccnz .LBB0_2045
	s_waitcnt vmcnt(0)
	s_waitcnt lgkmcnt(0)
	s_barrier
	s_and_saveexec_b64 s[0:1], s[78:79]
	s_cbranch_execz .LBB0_2044
	v_mov_b32_e32 v1, 0x22160
	s_waitcnt vmcnt(0) lgkmcnt(0)
	ds_read_b32 v2, v1
	v_mov_b32_e32 v3, 1
	v_mov_b32_e32 v4, s99
	v_and_b32_e32 v5, 0xffff, v4
	v_lshrrev_b32_e32 v6, 16, v4
	global_atomic_add v7, v5, v3, s[100:101] sc0
	buffer_inv sc1
	v_lshrrev_b32_e32 v8, 7, v5
	v_sub_u32_e32 v8, s98, v8
	v_add_u32_e32 v8, 31, v8
	v_lshrrev_b32_e32 v8, 5, v8
	v_mov_b32_e32 v9, s98
	v_min_u32_e32 v9, 32, v9
	v_mov_b32_e32 v10, 0
	s_waitcnt lgkmcnt(0)
	v_add_u32_e32 v2, 1, v2
	ds_write_b32 v1, v2
	v_mul_lo_u32 v8, v8, v2
	v_mul_lo_u32 v9, v9, v2
	s_waitcnt vmcnt(0)
	v_add_u32_e32 v7, 1, v7
	v_cmp_eq_u32_e32 vcc, v7, v8
	s_cbranch_vccz .Lgb_poll_13
	s_mov_b64 exec, -1
	v_mbcnt_lo_u32_b32 v4, -1, 0
	v_mbcnt_hi_u32_b32 v4, -1, v4
	v_lshlrev_b32_e32 v4, 7, v4
	v_add_u32_e32 v4, 0x1000, v4
	v_mov_b32_e32 v3, 1
	global_atomic_add v4, v3, s[100:101]
	s_mov_b64 exec, 1
